# top-k: sampled 12-bit bracket (quarter of the key registers) verified by two full counts, then exact descent below it; rows with >=20 key registers only
# speedup vs baseline: 1.0031x; 1.0031x over previous
.Ltk0_e32:
	s_movk_i32 s11, 64
	s_cmp_eq_u32 s33, 30
	s_cselect_b32 s11, 66, s11
	s_cmp_eq_u32 s33, 29
	s_cselect_b32 s11, 68, s11
	s_cmp_eq_u32 s33, 28
	s_cselect_b32 s11, 71, s11
.Ltk0_a32:
	s_or_b32 s6, s4, s5
	v_cmp_le_u32_e64 s[8:9], s6, v179
	v_cmp_le_u32_e64 s[12:13], s6, v187
	v_cmp_le_u32_e64 s[16:17], s6, v192
	v_cndmask_b32_e64 v8, 0, 1, s[8:9]
	v_cmp_le_u32_e64 s[8:9], s6, v196
	v_addc_co_u32_e64 v8, s[20:21], 0, v8, s[12:13]
	v_cmp_le_u32_e64 s[12:13], s6, v207
	v_addc_co_u32_e64 v8, s[20:21], 0, v8, s[16:17]
	v_cmp_le_u32_e64 s[16:17], s6, v211
	v_addc_co_u32_e64 v8, s[20:21], 0, v8, s[8:9]
	v_cmp_le_u32_e64 s[8:9], s6, v215
	v_addc_co_u32_e64 v8, s[20:21], 0, v8, s[12:13]
	v_cmp_le_u32_e64 s[12:13], s6, v220
	v_addc_co_u32_e64 v8, s[20:21], 0, v8, s[16:17]
	v_addc_co_u32_e64 v8, s[20:21], 0, v8, s[8:9]
	v_addc_co_u32_e64 v8, s[20:21], 0, v8, s[12:13]
	v_and_b32_e32 v9, 8, v8
	v_cmp_ne_u32_e64 s[18:19], 0, v9
	v_and_b32_e32 v9, 4, v8
	v_cmp_ne_u32_e64 s[16:17], 0, v9
	v_and_b32_e32 v9, 2, v8
	v_cmp_ne_u32_e64 s[12:13], 0, v9
	v_and_b32_e32 v9, 1, v8
	v_cmp_ne_u32_e64 s[8:9], 0, v9
	s_bcnt1_i32_b64 s7, s[18:19]
	s_bcnt1_i32_b64 s3, s[16:17]
	s_lshl1_add_u32 s7, s7, s3
	s_bcnt1_i32_b64 s3, s[12:13]
	s_lshl1_add_u32 s7, s7, s3
	s_bcnt1_i32_b64 s3, s[8:9]
	s_lshl1_add_u32 s7, s7, s3
	s_cmp_lt_u32 s7, s11
	s_cselect_b32 s4, s4, s6
	s_lshr_b32 s5, s5, 1
	s_cmp_lg_u32 s5, 0x80000
	s_cbranch_scc1 .Ltk0_a32
	s_mov_b32 s10, s4
	s_add_u32 s6, s4, 0x100000
	s_cbranch_scc1 .Ltk0_f32
	s_mov_b32 s5, 0
.Ltk0_b32:
	v_cmp_le_u32_e64 s[8:9], s6, v172
	v_cmp_le_u32_e64 s[12:13], s6, v179
	v_cmp_le_u32_e64 s[16:17], s6, v181
	v_cndmask_b32_e64 v8, 0, 1, s[8:9]
	v_cmp_le_u32_e64 s[8:9], s6, v183
	v_addc_co_u32_e64 v8, s[20:21], 0, v8, s[12:13]
	v_cmp_le_u32_e64 s[12:13], s6, v185
	v_addc_co_u32_e64 v8, s[20:21], 0, v8, s[16:17]
	v_cmp_le_u32_e64 s[16:17], s6, v187
	v_addc_co_u32_e64 v8, s[20:21], 0, v8, s[8:9]
	v_cmp_le_u32_e64 s[8:9], s6, v189
	v_addc_co_u32_e64 v8, s[20:21], 0, v8, s[12:13]
	v_cmp_le_u32_e64 s[12:13], s6, v190
	v_addc_co_u32_e64 v8, s[20:21], 0, v8, s[16:17]
	v_cmp_le_u32_e64 s[16:17], s6, v191
	v_addc_co_u32_e64 v8, s[20:21], 0, v8, s[8:9]
	v_cmp_le_u32_e64 s[8:9], s6, v192
	v_addc_co_u32_e64 v8, s[20:21], 0, v8, s[12:13]
	v_cmp_le_u32_e64 s[12:13], s6, v193
	v_addc_co_u32_e64 v8, s[20:21], 0, v8, s[16:17]
	v_cmp_le_u32_e64 s[16:17], s6, v194
	v_addc_co_u32_e64 v8, s[20:21], 0, v8, s[8:9]
	v_cmp_le_u32_e64 s[8:9], s6, v195
	v_addc_co_u32_e64 v8, s[20:21], 0, v8, s[12:13]
	v_cmp_le_u32_e64 s[12:13], s6, v196
	v_addc_co_u32_e64 v8, s[20:21], 0, v8, s[16:17]
	v_cmp_le_u32_e64 s[16:17], s6, v198
	v_addc_co_u32_e64 v8, s[20:21], 0, v8, s[8:9]
	v_cmp_le_u32_e64 s[8:9], s6, v200
	v_addc_co_u32_e64 v8, s[20:21], 0, v8, s[12:13]
	v_cmp_le_u32_e64 s[12:13], s6, v206
	v_addc_co_u32_e64 v8, s[20:21], 0, v8, s[16:17]
	v_cmp_le_u32_e64 s[16:17], s6, v207
	v_addc_co_u32_e64 v8, s[20:21], 0, v8, s[8:9]
	v_cmp_le_u32_e64 s[8:9], s6, v208
	v_addc_co_u32_e64 v8, s[20:21], 0, v8, s[12:13]
	v_cmp_le_u32_e64 s[12:13], s6, v209
	v_addc_co_u32_e64 v8, s[20:21], 0, v8, s[16:17]
	v_cmp_le_u32_e64 s[16:17], s6, v210
	v_addc_co_u32_e64 v8, s[20:21], 0, v8, s[8:9]
	v_cmp_le_u32_e64 s[8:9], s6, v211
	v_addc_co_u32_e64 v8, s[20:21], 0, v8, s[12:13]
	v_cmp_le_u32_e64 s[12:13], s6, v212
	v_addc_co_u32_e64 v8, s[20:21], 0, v8, s[16:17]
	v_cmp_le_u32_e64 s[16:17], s6, v213
	v_addc_co_u32_e64 v8, s[20:21], 0, v8, s[8:9]
	v_cmp_le_u32_e64 s[8:9], s6, v214
	v_addc_co_u32_e64 v8, s[20:21], 0, v8, s[12:13]
	v_cmp_le_u32_e64 s[12:13], s6, v215
	v_addc_co_u32_e64 v8, s[20:21], 0, v8, s[16:17]
	v_cmp_le_u32_e64 s[16:17], s6, v216
	v_addc_co_u32_e64 v8, s[20:21], 0, v8, s[8:9]
	v_cmp_le_u32_e64 s[8:9], s6, v217
	v_addc_co_u32_e64 v8, s[20:21], 0, v8, s[12:13]
	v_cmp_le_u32_e64 s[12:13], s6, v219
	v_addc_co_u32_e64 v8, s[20:21], 0, v8, s[16:17]
	v_cmp_le_u32_e64 s[16:17], s6, v220
	v_addc_co_u32_e64 v8, s[20:21], 0, v8, s[8:9]
	v_cmp_le_u32_e64 s[8:9], s6, v221
	v_addc_co_u32_e64 v8, s[20:21], 0, v8, s[12:13]
	v_cmp_le_u32_e64 s[12:13], s6, v2
	v_addc_co_u32_e64 v8, s[20:21], 0, v8, s[16:17]
	v_addc_co_u32_e64 v8, s[20:21], 0, v8, s[8:9]
	v_addc_co_u32_e64 v8, s[20:21], 0, v8, s[12:13]
	v_and_b32_e32 v9, 32, v8
	v_cmp_ne_u32_e64 s[0:1], 0, v9
	v_and_b32_e32 v9, 16, v8
	v_cmp_ne_u32_e64 s[22:23], 0, v9
	v_and_b32_e32 v9, 8, v8
	v_cmp_ne_u32_e64 s[18:19], 0, v9
	v_and_b32_e32 v9, 4, v8
	v_cmp_ne_u32_e64 s[16:17], 0, v9
	v_and_b32_e32 v9, 2, v8
	v_cmp_ne_u32_e64 s[12:13], 0, v9
	v_and_b32_e32 v9, 1, v8
	v_cmp_ne_u32_e64 s[8:9], 0, v9
	s_bcnt1_i32_b64 s7, s[0:1]
	s_bcnt1_i32_b64 s3, s[22:23]
	s_lshl1_add_u32 s7, s7, s3
	s_bcnt1_i32_b64 s3, s[18:19]
	s_lshl1_add_u32 s7, s7, s3
	s_bcnt1_i32_b64 s3, s[16:17]
	s_lshl1_add_u32 s7, s7, s3
	s_bcnt1_i32_b64 s3, s[12:13]
	s_lshl1_add_u32 s7, s7, s3
	s_bcnt1_i32_b64 s3, s[8:9]
	s_lshl1_add_u32 s7, s7, s3
	s_cmp_lg_u32 s5, 0
	s_cbranch_scc1 .Ltk0_c32
	s_cmpk_ge_u32 s7, 0x100
	s_cbranch_scc1 .Ltk0_f32
	s_mov_b32 s6, s10
	s_mov_b32 s5, 1
	s_branch .Ltk0_b32
.Ltk0_c32:
	s_cmpk_lt_u32 s7, 0x100
	s_cbranch_scc1 .Ltk0_f32
	s_mov_b32 s4, s10
	s_cmpk_eq_u32 s7, 0x100
	s_cbranch_scc1 .Ltk0_x32
	s_mov_b32 s5, 0x80000
	s_branch .Ltk0_l32
.Ltk0_f32:
	s_mov_b32 s4, 0
	s_mov_b32 s5, 0x80000000

.Ltk0_e28:
	s_movk_i32 s11, 64
	s_cmp_eq_u32 s33, 26
	s_cselect_b32 s11, 66, s11
	s_cmp_eq_u32 s33, 25
	s_cselect_b32 s11, 69, s11
	s_cmp_eq_u32 s33, 24
	s_cselect_b32 s11, 72, s11
.Ltk0_a28:
	s_or_b32 s6, s4, s5
	v_cmp_le_u32_e64 s[8:9], s6, v179
	v_cmp_le_u32_e64 s[12:13], s6, v187
	v_cmp_le_u32_e64 s[16:17], s6, v192
	v_cndmask_b32_e64 v8, 0, 1, s[8:9]
	v_cmp_le_u32_e64 s[8:9], s6, v196
	v_addc_co_u32_e64 v8, s[20:21], 0, v8, s[12:13]
	v_cmp_le_u32_e64 s[12:13], s6, v207
	v_addc_co_u32_e64 v8, s[20:21], 0, v8, s[16:17]
	v_cmp_le_u32_e64 s[16:17], s6, v211
	v_addc_co_u32_e64 v8, s[20:21], 0, v8, s[8:9]
	v_cmp_le_u32_e64 s[8:9], s6, v215
	v_addc_co_u32_e64 v8, s[20:21], 0, v8, s[12:13]
	v_addc_co_u32_e64 v8, s[20:21], 0, v8, s[16:17]
	v_addc_co_u32_e64 v8, s[20:21], 0, v8, s[8:9]
	v_and_b32_e32 v9, 4, v8
	v_cmp_ne_u32_e64 s[16:17], 0, v9
	v_and_b32_e32 v9, 2, v8
	v_cmp_ne_u32_e64 s[12:13], 0, v9
	v_and_b32_e32 v9, 1, v8
	v_cmp_ne_u32_e64 s[8:9], 0, v9
	s_bcnt1_i32_b64 s7, s[16:17]
	s_bcnt1_i32_b64 s3, s[12:13]
	s_lshl1_add_u32 s7, s7, s3
	s_bcnt1_i32_b64 s3, s[8:9]
	s_lshl1_add_u32 s7, s7, s3
	s_cmp_lt_u32 s7, s11
	s_cselect_b32 s4, s4, s6
	s_lshr_b32 s5, s5, 1
	s_cmp_lg_u32 s5, 0x80000
	s_cbranch_scc1 .Ltk0_a28
	s_mov_b32 s10, s4
	s_add_u32 s6, s4, 0x100000
	s_cbranch_scc1 .Ltk0_f28
	s_mov_b32 s5, 0
.Ltk0_b28:
	v_cmp_le_u32_e64 s[8:9], s6, v172
	v_cmp_le_u32_e64 s[12:13], s6, v179
	v_cmp_le_u32_e64 s[16:17], s6, v181
	v_cndmask_b32_e64 v8, 0, 1, s[8:9]
	v_cmp_le_u32_e64 s[8:9], s6, v183
	v_addc_co_u32_e64 v8, s[20:21], 0, v8, s[12:13]
	v_cmp_le_u32_e64 s[12:13], s6, v185
	v_addc_co_u32_e64 v8, s[20:21], 0, v8, s[16:17]
	v_cmp_le_u32_e64 s[16:17], s6, v187
	v_addc_co_u32_e64 v8, s[20:21], 0, v8, s[8:9]
	v_cmp_le_u32_e64 s[8:9], s6, v189
	v_addc_co_u32_e64 v8, s[20:21], 0, v8, s[12:13]
	v_cmp_le_u32_e64 s[12:13], s6, v190
	v_addc_co_u32_e64 v8, s[20:21], 0, v8, s[16:17]
	v_cmp_le_u32_e64 s[16:17], s6, v191
	v_addc_co_u32_e64 v8, s[20:21], 0, v8, s[8:9]
	v_cmp_le_u32_e64 s[8:9], s6, v192
	v_addc_co_u32_e64 v8, s[20:21], 0, v8, s[12:13]
	v_cmp_le_u32_e64 s[12:13], s6, v193
	v_addc_co_u32_e64 v8, s[20:21], 0, v8, s[16:17]
	v_cmp_le_u32_e64 s[16:17], s6, v194
	v_addc_co_u32_e64 v8, s[20:21], 0, v8, s[8:9]
	v_cmp_le_u32_e64 s[8:9], s6, v195
	v_addc_co_u32_e64 v8, s[20:21], 0, v8, s[12:13]
	v_cmp_le_u32_e64 s[12:13], s6, v196
	v_addc_co_u32_e64 v8, s[20:21], 0, v8, s[16:17]
	v_cmp_le_u32_e64 s[16:17], s6, v198
	v_addc_co_u32_e64 v8, s[20:21], 0, v8, s[8:9]
	v_cmp_le_u32_e64 s[8:9], s6, v200
	v_addc_co_u32_e64 v8, s[20:21], 0, v8, s[12:13]
	v_cmp_le_u32_e64 s[12:13], s6, v206
	v_addc_co_u32_e64 v8, s[20:21], 0, v8, s[16:17]
	v_cmp_le_u32_e64 s[16:17], s6, v207
	v_addc_co_u32_e64 v8, s[20:21], 0, v8, s[8:9]
	v_cmp_le_u32_e64 s[8:9], s6, v208
	v_addc_co_u32_e64 v8, s[20:21], 0, v8, s[12:13]
	v_cmp_le_u32_e64 s[12:13], s6, v209
	v_addc_co_u32_e64 v8, s[20:21], 0, v8, s[16:17]
	v_cmp_le_u32_e64 s[16:17], s6, v210
	v_addc_co_u32_e64 v8, s[20:21], 0, v8, s[8:9]
	v_cmp_le_u32_e64 s[8:9], s6, v211
	v_addc_co_u32_e64 v8, s[20:21], 0, v8, s[12:13]
	v_cmp_le_u32_e64 s[12:13], s6, v212
	v_addc_co_u32_e64 v8, s[20:21], 0, v8, s[16:17]
	v_cmp_le_u32_e64 s[16:17], s6, v213
	v_addc_co_u32_e64 v8, s[20:21], 0, v8, s[8:9]
	v_cmp_le_u32_e64 s[8:9], s6, v214
	v_addc_co_u32_e64 v8, s[20:21], 0, v8, s[12:13]
	v_cmp_le_u32_e64 s[12:13], s6, v215
	v_addc_co_u32_e64 v8, s[20:21], 0, v8, s[16:17]
	v_cmp_le_u32_e64 s[16:17], s6, v216
	v_addc_co_u32_e64 v8, s[20:21], 0, v8, s[8:9]
	v_cmp_le_u32_e64 s[8:9], s6, v217
	v_addc_co_u32_e64 v8, s[20:21], 0, v8, s[12:13]
	v_addc_co_u32_e64 v8, s[20:21], 0, v8, s[16:17]
	v_addc_co_u32_e64 v8, s[20:21], 0, v8, s[8:9]
	v_and_b32_e32 v9, 16, v8
	v_cmp_ne_u32_e64 s[22:23], 0, v9
	v_and_b32_e32 v9, 8, v8
	v_cmp_ne_u32_e64 s[18:19], 0, v9
	v_and_b32_e32 v9, 4, v8
	v_cmp_ne_u32_e64 s[16:17], 0, v9
	v_and_b32_e32 v9, 2, v8
	v_cmp_ne_u32_e64 s[12:13], 0, v9
	v_and_b32_e32 v9, 1, v8
	v_cmp_ne_u32_e64 s[8:9], 0, v9
	s_bcnt1_i32_b64 s7, s[22:23]
	s_bcnt1_i32_b64 s3, s[18:19]
	s_lshl1_add_u32 s7, s7, s3
	s_bcnt1_i32_b64 s3, s[16:17]
	s_lshl1_add_u32 s7, s7, s3
	s_bcnt1_i32_b64 s3, s[12:13]
	s_lshl1_add_u32 s7, s7, s3
	s_bcnt1_i32_b64 s3, s[8:9]
	s_lshl1_add_u32 s7, s7, s3
	s_cmp_lg_u32 s5, 0
	s_cbranch_scc1 .Ltk0_c28
	s_cmpk_ge_u32 s7, 0x100
	s_cbranch_scc1 .Ltk0_f28
	s_mov_b32 s6, s10
	s_mov_b32 s5, 1
	s_branch .Ltk0_b28

.Ltk0_e24:
	s_movk_i32 s11, 64
	s_cmp_eq_u32 s33, 22
	s_cselect_b32 s11, 67, s11
	s_cmp_eq_u32 s33, 21
	s_cselect_b32 s11, 70, s11
	s_cmp_eq_u32 s33, 20
	s_cselect_b32 s11, 73, s11
.Ltk0_a24:
	s_or_b32 s6, s4, s5
	v_cmp_le_u32_e64 s[8:9], s6, v179
	v_cmp_le_u32_e64 s[12:13], s6, v187
	v_cmp_le_u32_e64 s[16:17], s6, v192
	v_cndmask_b32_e64 v8, 0, 1, s[8:9]
	v_cmp_le_u32_e64 s[8:9], s6, v196
	v_addc_co_u32_e64 v8, s[20:21], 0, v8, s[12:13]
	v_cmp_le_u32_e64 s[12:13], s6, v207
	v_addc_co_u32_e64 v8, s[20:21], 0, v8, s[16:17]
	v_cmp_le_u32_e64 s[16:17], s6, v211
	v_addc_co_u32_e64 v8, s[20:21], 0, v8, s[8:9]
	v_addc_co_u32_e64 v8, s[20:21], 0, v8, s[12:13]
	v_addc_co_u32_e64 v8, s[20:21], 0, v8, s[16:17]
	v_and_b32_e32 v9, 4, v8
	v_cmp_ne_u32_e64 s[16:17], 0, v9
	v_and_b32_e32 v9, 2, v8
	v_cmp_ne_u32_e64 s[12:13], 0, v9
	v_and_b32_e32 v9, 1, v8
	v_cmp_ne_u32_e64 s[8:9], 0, v9
	s_bcnt1_i32_b64 s7, s[16:17]
	s_bcnt1_i32_b64 s3, s[12:13]
	s_lshl1_add_u32 s7, s7, s3
	s_bcnt1_i32_b64 s3, s[8:9]
	s_lshl1_add_u32 s7, s7, s3
	s_cmp_lt_u32 s7, s11
	s_cselect_b32 s4, s4, s6
	s_lshr_b32 s5, s5, 1
	s_cmp_lg_u32 s5, 0x80000
	s_cbranch_scc1 .Ltk0_a24
	s_mov_b32 s10, s4
	s_add_u32 s6, s4, 0x100000
	s_cbranch_scc1 .Ltk0_f24
	s_mov_b32 s5, 0
.Ltk0_b24:
	v_cmp_le_u32_e64 s[8:9], s6, v172
	v_cmp_le_u32_e64 s[12:13], s6, v179
	v_cmp_le_u32_e64 s[16:17], s6, v181
	v_cndmask_b32_e64 v8, 0, 1, s[8:9]
	v_cmp_le_u32_e64 s[8:9], s6, v183
	v_addc_co_u32_e64 v8, s[20:21], 0, v8, s[12:13]
	v_cmp_le_u32_e64 s[12:13], s6, v185
	v_addc_co_u32_e64 v8, s[20:21], 0, v8, s[16:17]
	v_cmp_le_u32_e64 s[16:17], s6, v187
	v_addc_co_u32_e64 v8, s[20:21], 0, v8, s[8:9]
	v_cmp_le_u32_e64 s[8:9], s6, v189
	v_addc_co_u32_e64 v8, s[20:21], 0, v8, s[12:13]
	v_cmp_le_u32_e64 s[12:13], s6, v190
	v_addc_co_u32_e64 v8, s[20:21], 0, v8, s[16:17]
	v_cmp_le_u32_e64 s[16:17], s6, v191
	v_addc_co_u32_e64 v8, s[20:21], 0, v8, s[8:9]
	v_cmp_le_u32_e64 s[8:9], s6, v192
	v_addc_co_u32_e64 v8, s[20:21], 0, v8, s[12:13]
	v_cmp_le_u32_e64 s[12:13], s6, v193
	v_addc_co_u32_e64 v8, s[20:21], 0, v8, s[16:17]
	v_cmp_le_u32_e64 s[16:17], s6, v194
	v_addc_co_u32_e64 v8, s[20:21], 0, v8, s[8:9]
	v_cmp_le_u32_e64 s[8:9], s6, v195
	v_addc_co_u32_e64 v8, s[20:21], 0, v8, s[12:13]
	v_cmp_le_u32_e64 s[12:13], s6, v196
	v_addc_co_u32_e64 v8, s[20:21], 0, v8, s[16:17]
	v_cmp_le_u32_e64 s[16:17], s6, v198
	v_addc_co_u32_e64 v8, s[20:21], 0, v8, s[8:9]
	v_cmp_le_u32_e64 s[8:9], s6, v200
	v_addc_co_u32_e64 v8, s[20:21], 0, v8, s[12:13]
	v_cmp_le_u32_e64 s[12:13], s6, v206
	v_addc_co_u32_e64 v8, s[20:21], 0, v8, s[16:17]
	v_cmp_le_u32_e64 s[16:17], s6, v207
	v_addc_co_u32_e64 v8, s[20:21], 0, v8, s[8:9]
	v_cmp_le_u32_e64 s[8:9], s6, v208
	v_addc_co_u32_e64 v8, s[20:21], 0, v8, s[12:13]
	v_cmp_le_u32_e64 s[12:13], s6, v209
	v_addc_co_u32_e64 v8, s[20:21], 0, v8, s[16:17]
	v_cmp_le_u32_e64 s[16:17], s6, v210
	v_addc_co_u32_e64 v8, s[20:21], 0, v8, s[8:9]
	v_cmp_le_u32_e64 s[8:9], s6, v211
	v_addc_co_u32_e64 v8, s[20:21], 0, v8, s[12:13]
	v_cmp_le_u32_e64 s[12:13], s6, v212
	v_addc_co_u32_e64 v8, s[20:21], 0, v8, s[16:17]
	v_cmp_le_u32_e64 s[16:17], s6, v213
	v_addc_co_u32_e64 v8, s[20:21], 0, v8, s[8:9]
	v_addc_co_u32_e64 v8, s[20:21], 0, v8, s[12:13]
	v_addc_co_u32_e64 v8, s[20:21], 0, v8, s[16:17]
	v_and_b32_e32 v9, 16, v8
	v_cmp_ne_u32_e64 s[22:23], 0, v9
	v_and_b32_e32 v9, 8, v8
	v_cmp_ne_u32_e64 s[18:19], 0, v9
	v_and_b32_e32 v9, 4, v8
	v_cmp_ne_u32_e64 s[16:17], 0, v9
	v_and_b32_e32 v9, 2, v8
	v_cmp_ne_u32_e64 s[12:13], 0, v9
	v_and_b32_e32 v9, 1, v8
	v_cmp_ne_u32_e64 s[8:9], 0, v9
	s_bcnt1_i32_b64 s7, s[22:23]
	s_bcnt1_i32_b64 s3, s[18:19]
	s_lshl1_add_u32 s7, s7, s3
	s_bcnt1_i32_b64 s3, s[16:17]
	s_lshl1_add_u32 s7, s7, s3
	s_bcnt1_i32_b64 s3, s[12:13]
	s_lshl1_add_u32 s7, s7, s3
	s_bcnt1_i32_b64 s3, s[8:9]
	s_lshl1_add_u32 s7, s7, s3
	s_cmp_lg_u32 s5, 0
	s_cbranch_scc1 .Ltk0_c24
	s_cmpk_ge_u32 s7, 0x100
	s_cbranch_scc1 .Ltk0_f24
	s_mov_b32 s6, s10
	s_mov_b32 s5, 1
	s_branch .Ltk0_b24

.Ltk0_e20:
	s_movk_i32 s11, 64
	s_cmp_eq_u32 s33, 18
	s_cselect_b32 s11, 67, s11
	s_cmp_eq_u32 s33, 17
	s_cselect_b32 s11, 71, s11
	s_cmp_eq_u32 s33, 16
	s_cselect_b32 s11, 75, s11
.Ltk0_a20:
	s_or_b32 s6, s4, s5
	v_cmp_le_u32_e64 s[8:9], s6, v179
	v_cmp_le_u32_e64 s[12:13], s6, v187
	v_cmp_le_u32_e64 s[16:17], s6, v192
	v_cndmask_b32_e64 v8, 0, 1, s[8:9]
	v_cmp_le_u32_e64 s[8:9], s6, v196
	v_addc_co_u32_e64 v8, s[20:21], 0, v8, s[12:13]
	v_cmp_le_u32_e64 s[12:13], s6, v207
	v_addc_co_u32_e64 v8, s[20:21], 0, v8, s[16:17]
	v_addc_co_u32_e64 v8, s[20:21], 0, v8, s[8:9]
	v_addc_co_u32_e64 v8, s[20:21], 0, v8, s[12:13]
	v_and_b32_e32 v9, 4, v8
	v_cmp_ne_u32_e64 s[16:17], 0, v9
	v_and_b32_e32 v9, 2, v8
	v_cmp_ne_u32_e64 s[12:13], 0, v9
	v_and_b32_e32 v9, 1, v8
	v_cmp_ne_u32_e64 s[8:9], 0, v9
	s_bcnt1_i32_b64 s7, s[16:17]
	s_bcnt1_i32_b64 s3, s[12:13]
	s_lshl1_add_u32 s7, s7, s3
	s_bcnt1_i32_b64 s3, s[8:9]
	s_lshl1_add_u32 s7, s7, s3
	s_cmp_lt_u32 s7, s11
	s_cselect_b32 s4, s4, s6
	s_lshr_b32 s5, s5, 1
	s_cmp_lg_u32 s5, 0x80000
	s_cbranch_scc1 .Ltk0_a20
	s_mov_b32 s10, s4
	s_add_u32 s6, s4, 0x100000
	s_cbranch_scc1 .Ltk0_f20
	s_mov_b32 s5, 0
.Ltk0_b20:
	v_cmp_le_u32_e64 s[8:9], s6, v172
	v_cmp_le_u32_e64 s[12:13], s6, v179
	v_cmp_le_u32_e64 s[16:17], s6, v181
	v_cndmask_b32_e64 v8, 0, 1, s[8:9]
	v_cmp_le_u32_e64 s[8:9], s6, v183
	v_addc_co_u32_e64 v8, s[20:21], 0, v8, s[12:13]
	v_cmp_le_u32_e64 s[12:13], s6, v185
	v_addc_co_u32_e64 v8, s[20:21], 0, v8, s[16:17]
	v_cmp_le_u32_e64 s[16:17], s6, v187
	v_addc_co_u32_e64 v8, s[20:21], 0, v8, s[8:9]
	v_cmp_le_u32_e64 s[8:9], s6, v189
	v_addc_co_u32_e64 v8, s[20:21], 0, v8, s[12:13]
	v_cmp_le_u32_e64 s[12:13], s6, v190
	v_addc_co_u32_e64 v8, s[20:21], 0, v8, s[16:17]
	v_cmp_le_u32_e64 s[16:17], s6, v191
	v_addc_co_u32_e64 v8, s[20:21], 0, v8, s[8:9]
	v_cmp_le_u32_e64 s[8:9], s6, v192
	v_addc_co_u32_e64 v8, s[20:21], 0, v8, s[12:13]
	v_cmp_le_u32_e64 s[12:13], s6, v193
	v_addc_co_u32_e64 v8, s[20:21], 0, v8, s[16:17]
	v_cmp_le_u32_e64 s[16:17], s6, v194
	v_addc_co_u32_e64 v8, s[20:21], 0, v8, s[8:9]
	v_cmp_le_u32_e64 s[8:9], s6, v195
	v_addc_co_u32_e64 v8, s[20:21], 0, v8, s[12:13]
	v_cmp_le_u32_e64 s[12:13], s6, v196
	v_addc_co_u32_e64 v8, s[20:21], 0, v8, s[16:17]
	v_cmp_le_u32_e64 s[16:17], s6, v198
	v_addc_co_u32_e64 v8, s[20:21], 0, v8, s[8:9]
	v_cmp_le_u32_e64 s[8:9], s6, v200
	v_addc_co_u32_e64 v8, s[20:21], 0, v8, s[12:13]
	v_cmp_le_u32_e64 s[12:13], s6, v206
	v_addc_co_u32_e64 v8, s[20:21], 0, v8, s[16:17]
	v_cmp_le_u32_e64 s[16:17], s6, v207
	v_addc_co_u32_e64 v8, s[20:21], 0, v8, s[8:9]
	v_cmp_le_u32_e64 s[8:9], s6, v208
	v_addc_co_u32_e64 v8, s[20:21], 0, v8, s[12:13]
	v_cmp_le_u32_e64 s[12:13], s6, v209
	v_addc_co_u32_e64 v8, s[20:21], 0, v8, s[16:17]
	v_addc_co_u32_e64 v8, s[20:21], 0, v8, s[8:9]
	v_addc_co_u32_e64 v8, s[20:21], 0, v8, s[12:13]
	v_and_b32_e32 v9, 16, v8
	v_cmp_ne_u32_e64 s[22:23], 0, v9
	v_and_b32_e32 v9, 8, v8
	v_cmp_ne_u32_e64 s[18:19], 0, v9
	v_and_b32_e32 v9, 4, v8
	v_cmp_ne_u32_e64 s[16:17], 0, v9
	v_and_b32_e32 v9, 2, v8
	v_cmp_ne_u32_e64 s[12:13], 0, v9
	v_and_b32_e32 v9, 1, v8
	v_cmp_ne_u32_e64 s[8:9], 0, v9
	s_bcnt1_i32_b64 s7, s[22:23]
	s_bcnt1_i32_b64 s3, s[18:19]
	s_lshl1_add_u32 s7, s7, s3
	s_bcnt1_i32_b64 s3, s[16:17]
	s_lshl1_add_u32 s7, s7, s3
	s_bcnt1_i32_b64 s3, s[12:13]
	s_lshl1_add_u32 s7, s7, s3
	s_bcnt1_i32_b64 s3, s[8:9]
	s_lshl1_add_u32 s7, s7, s3
	s_cmp_lg_u32 s5, 0
	s_cbranch_scc1 .Ltk0_c20
	s_cmpk_ge_u32 s7, 0x100
	s_cbranch_scc1 .Ltk0_f20
	s_mov_b32 s6, s10
	s_mov_b32 s5, 1
	s_branch .Ltk0_b20

.Ltk1_a32:
	s_or_b32 s6, s4, s5
	v_cmp_le_u32_e64 s[8:9], s6, v142
	v_cmp_le_u32_e64 s[12:13], s6, v150
	v_cmp_le_u32_e64 s[16:17], s6, v155
	v_cndmask_b32_e64 v8, 0, 1, s[8:9]
	v_cmp_le_u32_e64 s[8:9], s6, v159
	v_addc_co_u32_e64 v8, s[20:21], 0, v8, s[12:13]
	v_cmp_le_u32_e64 s[12:13], s6, v171
	v_addc_co_u32_e64 v8, s[20:21], 0, v8, s[16:17]
	v_cmp_le_u32_e64 s[16:17], s6, v184
	v_addc_co_u32_e64 v8, s[20:21], 0, v8, s[8:9]
	v_cmp_le_u32_e64 s[8:9], s6, v199
	v_addc_co_u32_e64 v8, s[20:21], 0, v8, s[12:13]
	v_cmp_le_u32_e64 s[12:13], s6, v204
	v_addc_co_u32_e64 v8, s[20:21], 0, v8, s[16:17]
	v_addc_co_u32_e64 v8, s[20:21], 0, v8, s[8:9]
	v_addc_co_u32_e64 v8, s[20:21], 0, v8, s[12:13]
	v_and_b32_e32 v9, 8, v8
	v_cmp_ne_u32_e64 s[18:19], 0, v9
	v_and_b32_e32 v9, 4, v8
	v_cmp_ne_u32_e64 s[16:17], 0, v9
	v_and_b32_e32 v9, 2, v8
	v_cmp_ne_u32_e64 s[12:13], 0, v9
	v_and_b32_e32 v9, 1, v8
	v_cmp_ne_u32_e64 s[8:9], 0, v9
	s_bcnt1_i32_b64 s7, s[18:19]
	s_bcnt1_i32_b64 s3, s[16:17]
	s_lshl1_add_u32 s7, s7, s3
	s_bcnt1_i32_b64 s3, s[12:13]
	s_lshl1_add_u32 s7, s7, s3
	s_bcnt1_i32_b64 s3, s[8:9]
	s_lshl1_add_u32 s7, s7, s3
	s_cmp_lt_u32 s7, s11
	s_cselect_b32 s4, s4, s6
	s_lshr_b32 s5, s5, 1
	s_cmp_lg_u32 s5, 0x80000
	s_cbranch_scc1 .Ltk1_a32
	s_mov_b32 s10, s4
	s_add_u32 s6, s4, 0x100000
	s_cbranch_scc1 .Ltk1_f32
	s_mov_b32 s5, 0
.Ltk1_b32:
	v_cmp_le_u32_e64 s[8:9], s6, v140
	v_cmp_le_u32_e64 s[12:13], s6, v142
	v_cmp_le_u32_e64 s[16:17], s6, v144
	v_cndmask_b32_e64 v8, 0, 1, s[8:9]
	v_cmp_le_u32_e64 s[8:9], s6, v146
	v_addc_co_u32_e64 v8, s[20:21], 0, v8, s[12:13]
	v_cmp_le_u32_e64 s[12:13], s6, v148
	v_addc_co_u32_e64 v8, s[20:21], 0, v8, s[16:17]
	v_cmp_le_u32_e64 s[16:17], s6, v150
	v_addc_co_u32_e64 v8, s[20:21], 0, v8, s[8:9]
	v_cmp_le_u32_e64 s[8:9], s6, v152
	v_addc_co_u32_e64 v8, s[20:21], 0, v8, s[12:13]
	v_cmp_le_u32_e64 s[12:13], s6, v153
	v_addc_co_u32_e64 v8, s[20:21], 0, v8, s[16:17]
	v_cmp_le_u32_e64 s[16:17], s6, v154
	v_addc_co_u32_e64 v8, s[20:21], 0, v8, s[8:9]
	v_cmp_le_u32_e64 s[8:9], s6, v155
	v_addc_co_u32_e64 v8, s[20:21], 0, v8, s[12:13]
	v_cmp_le_u32_e64 s[12:13], s6, v156
	v_addc_co_u32_e64 v8, s[20:21], 0, v8, s[16:17]
	v_cmp_le_u32_e64 s[16:17], s6, v157
	v_addc_co_u32_e64 v8, s[20:21], 0, v8, s[8:9]
	v_cmp_le_u32_e64 s[8:9], s6, v158
	v_addc_co_u32_e64 v8, s[20:21], 0, v8, s[12:13]
	v_cmp_le_u32_e64 s[12:13], s6, v159
	v_addc_co_u32_e64 v8, s[20:21], 0, v8, s[16:17]
	v_cmp_le_u32_e64 s[16:17], s6, v161
	v_addc_co_u32_e64 v8, s[20:21], 0, v8, s[8:9]
	v_cmp_le_u32_e64 s[8:9], s6, v164
	v_addc_co_u32_e64 v8, s[20:21], 0, v8, s[12:13]
	v_cmp_le_u32_e64 s[12:13], s6, v170
	v_addc_co_u32_e64 v8, s[20:21], 0, v8, s[16:17]
	v_cmp_le_u32_e64 s[16:17], s6, v171
	v_addc_co_u32_e64 v8, s[20:21], 0, v8, s[8:9]
	v_cmp_le_u32_e64 s[8:9], s6, v173
	v_addc_co_u32_e64 v8, s[20:21], 0, v8, s[12:13]
	v_cmp_le_u32_e64 s[12:13], s6, v180
	v_addc_co_u32_e64 v8, s[20:21], 0, v8, s[16:17]
	v_cmp_le_u32_e64 s[16:17], s6, v182
	v_addc_co_u32_e64 v8, s[20:21], 0, v8, s[8:9]
	v_cmp_le_u32_e64 s[8:9], s6, v184
	v_addc_co_u32_e64 v8, s[20:21], 0, v8, s[12:13]
	v_cmp_le_u32_e64 s[12:13], s6, v186
	v_addc_co_u32_e64 v8, s[20:21], 0, v8, s[16:17]
	v_cmp_le_u32_e64 s[16:17], s6, v188
	v_addc_co_u32_e64 v8, s[20:21], 0, v8, s[8:9]
	v_cmp_le_u32_e64 s[8:9], s6, v197
	v_addc_co_u32_e64 v8, s[20:21], 0, v8, s[12:13]
	v_cmp_le_u32_e64 s[12:13], s6, v199
	v_addc_co_u32_e64 v8, s[20:21], 0, v8, s[16:17]
	v_cmp_le_u32_e64 s[16:17], s6, v201
	v_addc_co_u32_e64 v8, s[20:21], 0, v8, s[8:9]
	v_cmp_le_u32_e64 s[8:9], s6, v202
	v_addc_co_u32_e64 v8, s[20:21], 0, v8, s[12:13]
	v_cmp_le_u32_e64 s[12:13], s6, v203
	v_addc_co_u32_e64 v8, s[20:21], 0, v8, s[16:17]
	v_cmp_le_u32_e64 s[16:17], s6, v204
	v_addc_co_u32_e64 v8, s[20:21], 0, v8, s[8:9]
	v_cmp_le_u32_e64 s[8:9], s6, v205
	v_addc_co_u32_e64 v8, s[20:21], 0, v8, s[12:13]
	v_cmp_le_u32_e64 s[12:13], s6, v7
	v_addc_co_u32_e64 v8, s[20:21], 0, v8, s[16:17]
	v_addc_co_u32_e64 v8, s[20:21], 0, v8, s[8:9]
	v_addc_co_u32_e64 v8, s[20:21], 0, v8, s[12:13]
	v_and_b32_e32 v9, 32, v8
	v_cmp_ne_u32_e64 s[0:1], 0, v9
	v_and_b32_e32 v9, 16, v8
	v_cmp_ne_u32_e64 s[22:23], 0, v9
	v_and_b32_e32 v9, 8, v8
	v_cmp_ne_u32_e64 s[18:19], 0, v9
	v_and_b32_e32 v9, 4, v8
	v_cmp_ne_u32_e64 s[16:17], 0, v9
	v_and_b32_e32 v9, 2, v8
	v_cmp_ne_u32_e64 s[12:13], 0, v9
	v_and_b32_e32 v9, 1, v8
	v_cmp_ne_u32_e64 s[8:9], 0, v9
	s_bcnt1_i32_b64 s7, s[0:1]
	s_bcnt1_i32_b64 s3, s[22:23]
	s_lshl1_add_u32 s7, s7, s3
	s_bcnt1_i32_b64 s3, s[18:19]
	s_lshl1_add_u32 s7, s7, s3
	s_bcnt1_i32_b64 s3, s[16:17]
	s_lshl1_add_u32 s7, s7, s3
	s_bcnt1_i32_b64 s3, s[12:13]
	s_lshl1_add_u32 s7, s7, s3
	s_bcnt1_i32_b64 s3, s[8:9]
	s_lshl1_add_u32 s7, s7, s3
	s_cmp_lg_u32 s5, 0
	s_cbranch_scc1 .Ltk1_c32
	s_cmpk_ge_u32 s7, 0x100
	s_cbranch_scc1 .Ltk1_f32
	s_mov_b32 s6, s10
	s_mov_b32 s5, 1
	s_branch .Ltk1_b32

.Ltk1_a28:
	s_or_b32 s6, s4, s5
	v_cmp_le_u32_e64 s[8:9], s6, v142
	v_cmp_le_u32_e64 s[12:13], s6, v150
	v_cmp_le_u32_e64 s[16:17], s6, v155
	v_cndmask_b32_e64 v8, 0, 1, s[8:9]
	v_cmp_le_u32_e64 s[8:9], s6, v159
	v_addc_co_u32_e64 v8, s[20:21], 0, v8, s[12:13]
	v_cmp_le_u32_e64 s[12:13], s6, v171
	v_addc_co_u32_e64 v8, s[20:21], 0, v8, s[16:17]
	v_cmp_le_u32_e64 s[16:17], s6, v184
	v_addc_co_u32_e64 v8, s[20:21], 0, v8, s[8:9]
	v_cmp_le_u32_e64 s[8:9], s6, v199
	v_addc_co_u32_e64 v8, s[20:21], 0, v8, s[12:13]
	v_addc_co_u32_e64 v8, s[20:21], 0, v8, s[16:17]
	v_addc_co_u32_e64 v8, s[20:21], 0, v8, s[8:9]
	v_and_b32_e32 v9, 4, v8
	v_cmp_ne_u32_e64 s[16:17], 0, v9
	v_and_b32_e32 v9, 2, v8
	v_cmp_ne_u32_e64 s[12:13], 0, v9
	v_and_b32_e32 v9, 1, v8
	v_cmp_ne_u32_e64 s[8:9], 0, v9
	s_bcnt1_i32_b64 s7, s[16:17]
	s_bcnt1_i32_b64 s3, s[12:13]
	s_lshl1_add_u32 s7, s7, s3
	s_bcnt1_i32_b64 s3, s[8:9]
	s_lshl1_add_u32 s7, s7, s3
	s_cmp_lt_u32 s7, s11
	s_cselect_b32 s4, s4, s6
	s_lshr_b32 s5, s5, 1
	s_cmp_lg_u32 s5, 0x80000
	s_cbranch_scc1 .Ltk1_a28
	s_mov_b32 s10, s4
	s_add_u32 s6, s4, 0x100000
	s_cbranch_scc1 .Ltk1_f28
	s_mov_b32 s5, 0
.Ltk1_b28:
	v_cmp_le_u32_e64 s[8:9], s6, v140
	v_cmp_le_u32_e64 s[12:13], s6, v142
	v_cmp_le_u32_e64 s[16:17], s6, v144
	v_cndmask_b32_e64 v8, 0, 1, s[8:9]
	v_cmp_le_u32_e64 s[8:9], s6, v146
	v_addc_co_u32_e64 v8, s[20:21], 0, v8, s[12:13]
	v_cmp_le_u32_e64 s[12:13], s6, v148
	v_addc_co_u32_e64 v8, s[20:21], 0, v8, s[16:17]
	v_cmp_le_u32_e64 s[16:17], s6, v150
	v_addc_co_u32_e64 v8, s[20:21], 0, v8, s[8:9]
	v_cmp_le_u32_e64 s[8:9], s6, v152
	v_addc_co_u32_e64 v8, s[20:21], 0, v8, s[12:13]
	v_cmp_le_u32_e64 s[12:13], s6, v153
	v_addc_co_u32_e64 v8, s[20:21], 0, v8, s[16:17]
	v_cmp_le_u32_e64 s[16:17], s6, v154
	v_addc_co_u32_e64 v8, s[20:21], 0, v8, s[8:9]
	v_cmp_le_u32_e64 s[8:9], s6, v155
	v_addc_co_u32_e64 v8, s[20:21], 0, v8, s[12:13]
	v_cmp_le_u32_e64 s[12:13], s6, v156
	v_addc_co_u32_e64 v8, s[20:21], 0, v8, s[16:17]
	v_cmp_le_u32_e64 s[16:17], s6, v157
	v_addc_co_u32_e64 v8, s[20:21], 0, v8, s[8:9]
	v_cmp_le_u32_e64 s[8:9], s6, v158
	v_addc_co_u32_e64 v8, s[20:21], 0, v8, s[12:13]
	v_cmp_le_u32_e64 s[12:13], s6, v159
	v_addc_co_u32_e64 v8, s[20:21], 0, v8, s[16:17]
	v_cmp_le_u32_e64 s[16:17], s6, v161
	v_addc_co_u32_e64 v8, s[20:21], 0, v8, s[8:9]
	v_cmp_le_u32_e64 s[8:9], s6, v164
	v_addc_co_u32_e64 v8, s[20:21], 0, v8, s[12:13]
	v_cmp_le_u32_e64 s[12:13], s6, v170
	v_addc_co_u32_e64 v8, s[20:21], 0, v8, s[16:17]
	v_cmp_le_u32_e64 s[16:17], s6, v171
	v_addc_co_u32_e64 v8, s[20:21], 0, v8, s[8:9]
	v_cmp_le_u32_e64 s[8:9], s6, v173
	v_addc_co_u32_e64 v8, s[20:21], 0, v8, s[12:13]
	v_cmp_le_u32_e64 s[12:13], s6, v180
	v_addc_co_u32_e64 v8, s[20:21], 0, v8, s[16:17]
	v_cmp_le_u32_e64 s[16:17], s6, v182
	v_addc_co_u32_e64 v8, s[20:21], 0, v8, s[8:9]
	v_cmp_le_u32_e64 s[8:9], s6, v184
	v_addc_co_u32_e64 v8, s[20:21], 0, v8, s[12:13]
	v_cmp_le_u32_e64 s[12:13], s6, v186
	v_addc_co_u32_e64 v8, s[20:21], 0, v8, s[16:17]
	v_cmp_le_u32_e64 s[16:17], s6, v188
	v_addc_co_u32_e64 v8, s[20:21], 0, v8, s[8:9]
	v_cmp_le_u32_e64 s[8:9], s6, v197
	v_addc_co_u32_e64 v8, s[20:21], 0, v8, s[12:13]
	v_cmp_le_u32_e64 s[12:13], s6, v199
	v_addc_co_u32_e64 v8, s[20:21], 0, v8, s[16:17]
	v_cmp_le_u32_e64 s[16:17], s6, v201
	v_addc_co_u32_e64 v8, s[20:21], 0, v8, s[8:9]
	v_cmp_le_u32_e64 s[8:9], s6, v202
	v_addc_co_u32_e64 v8, s[20:21], 0, v8, s[12:13]
	v_addc_co_u32_e64 v8, s[20:21], 0, v8, s[16:17]
	v_addc_co_u32_e64 v8, s[20:21], 0, v8, s[8:9]
	v_and_b32_e32 v9, 16, v8
	v_cmp_ne_u32_e64 s[22:23], 0, v9
	v_and_b32_e32 v9, 8, v8
	v_cmp_ne_u32_e64 s[18:19], 0, v9
	v_and_b32_e32 v9, 4, v8
	v_cmp_ne_u32_e64 s[16:17], 0, v9
	v_and_b32_e32 v9, 2, v8
	v_cmp_ne_u32_e64 s[12:13], 0, v9
	v_and_b32_e32 v9, 1, v8
	v_cmp_ne_u32_e64 s[8:9], 0, v9
	s_bcnt1_i32_b64 s7, s[22:23]
	s_bcnt1_i32_b64 s3, s[18:19]
	s_lshl1_add_u32 s7, s7, s3
	s_bcnt1_i32_b64 s3, s[16:17]
	s_lshl1_add_u32 s7, s7, s3
	s_bcnt1_i32_b64 s3, s[12:13]
	s_lshl1_add_u32 s7, s7, s3
	s_bcnt1_i32_b64 s3, s[8:9]
	s_lshl1_add_u32 s7, s7, s3
	s_cmp_lg_u32 s5, 0
	s_cbranch_scc1 .Ltk1_c28
	s_cmpk_ge_u32 s7, 0x100
	s_cbranch_scc1 .Ltk1_f28
	s_mov_b32 s6, s10
	s_mov_b32 s5, 1
	s_branch .Ltk1_b28

.Ltk1_a24:
	s_or_b32 s6, s4, s5
	v_cmp_le_u32_e64 s[8:9], s6, v142
	v_cmp_le_u32_e64 s[12:13], s6, v150
	v_cmp_le_u32_e64 s[16:17], s6, v155
	v_cndmask_b32_e64 v8, 0, 1, s[8:9]
	v_cmp_le_u32_e64 s[8:9], s6, v159
	v_addc_co_u32_e64 v8, s[20:21], 0, v8, s[12:13]
	v_cmp_le_u32_e64 s[12:13], s6, v171
	v_addc_co_u32_e64 v8, s[20:21], 0, v8, s[16:17]
	v_cmp_le_u32_e64 s[16:17], s6, v184
	v_addc_co_u32_e64 v8, s[20:21], 0, v8, s[8:9]
	v_addc_co_u32_e64 v8, s[20:21], 0, v8, s[12:13]
	v_addc_co_u32_e64 v8, s[20:21], 0, v8, s[16:17]
	v_and_b32_e32 v9, 4, v8
	v_cmp_ne_u32_e64 s[16:17], 0, v9
	v_and_b32_e32 v9, 2, v8
	v_cmp_ne_u32_e64 s[12:13], 0, v9
	v_and_b32_e32 v9, 1, v8
	v_cmp_ne_u32_e64 s[8:9], 0, v9
	s_bcnt1_i32_b64 s7, s[16:17]
	s_bcnt1_i32_b64 s3, s[12:13]
	s_lshl1_add_u32 s7, s7, s3
	s_bcnt1_i32_b64 s3, s[8:9]
	s_lshl1_add_u32 s7, s7, s3
	s_cmp_lt_u32 s7, s11
	s_cselect_b32 s4, s4, s6
	s_lshr_b32 s5, s5, 1
	s_cmp_lg_u32 s5, 0x80000
	s_cbranch_scc1 .Ltk1_a24
	s_mov_b32 s10, s4
	s_add_u32 s6, s4, 0x100000
	s_cbranch_scc1 .Ltk1_f24
	s_mov_b32 s5, 0
.Ltk1_b24:
	v_cmp_le_u32_e64 s[8:9], s6, v140
	v_cmp_le_u32_e64 s[12:13], s6, v142
	v_cmp_le_u32_e64 s[16:17], s6, v144
	v_cndmask_b32_e64 v8, 0, 1, s[8:9]
	v_cmp_le_u32_e64 s[8:9], s6, v146
	v_addc_co_u32_e64 v8, s[20:21], 0, v8, s[12:13]
	v_cmp_le_u32_e64 s[12:13], s6, v148
	v_addc_co_u32_e64 v8, s[20:21], 0, v8, s[16:17]
	v_cmp_le_u32_e64 s[16:17], s6, v150
	v_addc_co_u32_e64 v8, s[20:21], 0, v8, s[8:9]
	v_cmp_le_u32_e64 s[8:9], s6, v152
	v_addc_co_u32_e64 v8, s[20:21], 0, v8, s[12:13]
	v_cmp_le_u32_e64 s[12:13], s6, v153
	v_addc_co_u32_e64 v8, s[20:21], 0, v8, s[16:17]
	v_cmp_le_u32_e64 s[16:17], s6, v154
	v_addc_co_u32_e64 v8, s[20:21], 0, v8, s[8:9]
	v_cmp_le_u32_e64 s[8:9], s6, v155
	v_addc_co_u32_e64 v8, s[20:21], 0, v8, s[12:13]
	v_cmp_le_u32_e64 s[12:13], s6, v156
	v_addc_co_u32_e64 v8, s[20:21], 0, v8, s[16:17]
	v_cmp_le_u32_e64 s[16:17], s6, v157
	v_addc_co_u32_e64 v8, s[20:21], 0, v8, s[8:9]
	v_cmp_le_u32_e64 s[8:9], s6, v158
	v_addc_co_u32_e64 v8, s[20:21], 0, v8, s[12:13]
	v_cmp_le_u32_e64 s[12:13], s6, v159
	v_addc_co_u32_e64 v8, s[20:21], 0, v8, s[16:17]
	v_cmp_le_u32_e64 s[16:17], s6, v161
	v_addc_co_u32_e64 v8, s[20:21], 0, v8, s[8:9]
	v_cmp_le_u32_e64 s[8:9], s6, v164
	v_addc_co_u32_e64 v8, s[20:21], 0, v8, s[12:13]
	v_cmp_le_u32_e64 s[12:13], s6, v170
	v_addc_co_u32_e64 v8, s[20:21], 0, v8, s[16:17]
	v_cmp_le_u32_e64 s[16:17], s6, v171
	v_addc_co_u32_e64 v8, s[20:21], 0, v8, s[8:9]
	v_cmp_le_u32_e64 s[8:9], s6, v173
	v_addc_co_u32_e64 v8, s[20:21], 0, v8, s[12:13]
	v_cmp_le_u32_e64 s[12:13], s6, v180
	v_addc_co_u32_e64 v8, s[20:21], 0, v8, s[16:17]
	v_cmp_le_u32_e64 s[16:17], s6, v182
	v_addc_co_u32_e64 v8, s[20:21], 0, v8, s[8:9]
	v_cmp_le_u32_e64 s[8:9], s6, v184
	v_addc_co_u32_e64 v8, s[20:21], 0, v8, s[12:13]
	v_cmp_le_u32_e64 s[12:13], s6, v186
	v_addc_co_u32_e64 v8, s[20:21], 0, v8, s[16:17]
	v_cmp_le_u32_e64 s[16:17], s6, v188
	v_addc_co_u32_e64 v8, s[20:21], 0, v8, s[8:9]
	v_addc_co_u32_e64 v8, s[20:21], 0, v8, s[12:13]
	v_addc_co_u32_e64 v8, s[20:21], 0, v8, s[16:17]
	v_and_b32_e32 v9, 16, v8
	v_cmp_ne_u32_e64 s[22:23], 0, v9
	v_and_b32_e32 v9, 8, v8
	v_cmp_ne_u32_e64 s[18:19], 0, v9
	v_and_b32_e32 v9, 4, v8
	v_cmp_ne_u32_e64 s[16:17], 0, v9
	v_and_b32_e32 v9, 2, v8
	v_cmp_ne_u32_e64 s[12:13], 0, v9
	v_and_b32_e32 v9, 1, v8
	v_cmp_ne_u32_e64 s[8:9], 0, v9
	s_bcnt1_i32_b64 s7, s[22:23]
	s_bcnt1_i32_b64 s3, s[18:19]
	s_lshl1_add_u32 s7, s7, s3
	s_bcnt1_i32_b64 s3, s[16:17]
	s_lshl1_add_u32 s7, s7, s3
	s_bcnt1_i32_b64 s3, s[12:13]
	s_lshl1_add_u32 s7, s7, s3
	s_bcnt1_i32_b64 s3, s[8:9]
	s_lshl1_add_u32 s7, s7, s3
	s_cmp_lg_u32 s5, 0
	s_cbranch_scc1 .Ltk1_c24
	s_cmpk_ge_u32 s7, 0x100
	s_cbranch_scc1 .Ltk1_f24
	s_mov_b32 s6, s10
	s_mov_b32 s5, 1
	s_branch .Ltk1_b24

.Ltk1_a20:
	s_or_b32 s6, s4, s5
	v_cmp_le_u32_e64 s[8:9], s6, v142
	v_cmp_le_u32_e64 s[12:13], s6, v150
	v_cmp_le_u32_e64 s[16:17], s6, v155
	v_cndmask_b32_e64 v8, 0, 1, s[8:9]
	v_cmp_le_u32_e64 s[8:9], s6, v159
	v_addc_co_u32_e64 v8, s[20:21], 0, v8, s[12:13]
	v_cmp_le_u32_e64 s[12:13], s6, v171
	v_addc_co_u32_e64 v8, s[20:21], 0, v8, s[16:17]
	v_addc_co_u32_e64 v8, s[20:21], 0, v8, s[8:9]
	v_addc_co_u32_e64 v8, s[20:21], 0, v8, s[12:13]
	v_and_b32_e32 v9, 4, v8
	v_cmp_ne_u32_e64 s[16:17], 0, v9
	v_and_b32_e32 v9, 2, v8
	v_cmp_ne_u32_e64 s[12:13], 0, v9
	v_and_b32_e32 v9, 1, v8
	v_cmp_ne_u32_e64 s[8:9], 0, v9
	s_bcnt1_i32_b64 s7, s[16:17]
	s_bcnt1_i32_b64 s3, s[12:13]
	s_lshl1_add_u32 s7, s7, s3
	s_bcnt1_i32_b64 s3, s[8:9]
	s_lshl1_add_u32 s7, s7, s3
	s_cmp_lt_u32 s7, s11
	s_cselect_b32 s4, s4, s6
	s_lshr_b32 s5, s5, 1
	s_cmp_lg_u32 s5, 0x80000
	s_cbranch_scc1 .Ltk1_a20
	s_mov_b32 s10, s4
	s_add_u32 s6, s4, 0x100000
	s_cbranch_scc1 .Ltk1_f20
	s_mov_b32 s5, 0
.Ltk1_b20:
	v_cmp_le_u32_e64 s[8:9], s6, v140
	v_cmp_le_u32_e64 s[12:13], s6, v142
	v_cmp_le_u32_e64 s[16:17], s6, v144
	v_cndmask_b32_e64 v8, 0, 1, s[8:9]
	v_cmp_le_u32_e64 s[8:9], s6, v146
	v_addc_co_u32_e64 v8, s[20:21], 0, v8, s[12:13]
	v_cmp_le_u32_e64 s[12:13], s6, v148
	v_addc_co_u32_e64 v8, s[20:21], 0, v8, s[16:17]
	v_cmp_le_u32_e64 s[16:17], s6, v150
	v_addc_co_u32_e64 v8, s[20:21], 0, v8, s[8:9]
	v_cmp_le_u32_e64 s[8:9], s6, v152
	v_addc_co_u32_e64 v8, s[20:21], 0, v8, s[12:13]
	v_cmp_le_u32_e64 s[12:13], s6, v153
	v_addc_co_u32_e64 v8, s[20:21], 0, v8, s[16:17]
	v_cmp_le_u32_e64 s[16:17], s6, v154
	v_addc_co_u32_e64 v8, s[20:21], 0, v8, s[8:9]
	v_cmp_le_u32_e64 s[8:9], s6, v155
	v_addc_co_u32_e64 v8, s[20:21], 0, v8, s[12:13]
	v_cmp_le_u32_e64 s[12:13], s6, v156
	v_addc_co_u32_e64 v8, s[20:21], 0, v8, s[16:17]
	v_cmp_le_u32_e64 s[16:17], s6, v157
	v_addc_co_u32_e64 v8, s[20:21], 0, v8, s[8:9]
	v_cmp_le_u32_e64 s[8:9], s6, v158
	v_addc_co_u32_e64 v8, s[20:21], 0, v8, s[12:13]
	v_cmp_le_u32_e64 s[12:13], s6, v159
	v_addc_co_u32_e64 v8, s[20:21], 0, v8, s[16:17]
	v_cmp_le_u32_e64 s[16:17], s6, v161
	v_addc_co_u32_e64 v8, s[20:21], 0, v8, s[8:9]
	v_cmp_le_u32_e64 s[8:9], s6, v164
	v_addc_co_u32_e64 v8, s[20:21], 0, v8, s[12:13]
	v_cmp_le_u32_e64 s[12:13], s6, v170
	v_addc_co_u32_e64 v8, s[20:21], 0, v8, s[16:17]
	v_cmp_le_u32_e64 s[16:17], s6, v171
	v_addc_co_u32_e64 v8, s[20:21], 0, v8, s[8:9]
	v_cmp_le_u32_e64 s[8:9], s6, v173
	v_addc_co_u32_e64 v8, s[20:21], 0, v8, s[12:13]
	v_cmp_le_u32_e64 s[12:13], s6, v180
	v_addc_co_u32_e64 v8, s[20:21], 0, v8, s[16:17]
	v_addc_co_u32_e64 v8, s[20:21], 0, v8, s[8:9]
	v_addc_co_u32_e64 v8, s[20:21], 0, v8, s[12:13]
	v_and_b32_e32 v9, 16, v8
	v_cmp_ne_u32_e64 s[22:23], 0, v9
	v_and_b32_e32 v9, 8, v8
	v_cmp_ne_u32_e64 s[18:19], 0, v9
	v_and_b32_e32 v9, 4, v8
	v_cmp_ne_u32_e64 s[16:17], 0, v9
	v_and_b32_e32 v9, 2, v8
	v_cmp_ne_u32_e64 s[12:13], 0, v9
	v_and_b32_e32 v9, 1, v8
	v_cmp_ne_u32_e64 s[8:9], 0, v9
	s_bcnt1_i32_b64 s7, s[22:23]
	s_bcnt1_i32_b64 s3, s[18:19]
	s_lshl1_add_u32 s7, s7, s3
	s_bcnt1_i32_b64 s3, s[16:17]
	s_lshl1_add_u32 s7, s7, s3
	s_bcnt1_i32_b64 s3, s[12:13]
	s_lshl1_add_u32 s7, s7, s3
	s_bcnt1_i32_b64 s3, s[8:9]
	s_lshl1_add_u32 s7, s7, s3
	s_cmp_lg_u32 s5, 0
	s_cbranch_scc1 .Ltk1_c20
	s_cmpk_ge_u32 s7, 0x100
	s_cbranch_scc1 .Ltk1_f20
	s_mov_b32 s6, s10
	s_mov_b32 s5, 1
	s_branch .Ltk1_b20

.Ltk2_a32:
	s_or_b32 s6, s4, s5
	v_cmp_le_u32_e64 s[8:9], s6, v113
	v_cmp_le_u32_e64 s[12:13], s6, v121
	v_cmp_le_u32_e64 s[16:17], s6, v126
	v_cndmask_b32_e64 v8, 0, 1, s[8:9]
	v_cmp_le_u32_e64 s[8:9], s6, v130
	v_addc_co_u32_e64 v8, s[20:21], 0, v8, s[12:13]
	v_cmp_le_u32_e64 s[12:13], s6, v139
	v_addc_co_u32_e64 v8, s[20:21], 0, v8, s[16:17]
	v_cmp_le_u32_e64 s[16:17], s6, v147
	v_addc_co_u32_e64 v8, s[20:21], 0, v8, s[8:9]
	v_cmp_le_u32_e64 s[8:9], s6, v163
	v_addc_co_u32_e64 v8, s[20:21], 0, v8, s[12:13]
	v_cmp_le_u32_e64 s[12:13], s6, v168
	v_addc_co_u32_e64 v8, s[20:21], 0, v8, s[16:17]
	v_addc_co_u32_e64 v8, s[20:21], 0, v8, s[8:9]
	v_addc_co_u32_e64 v8, s[20:21], 0, v8, s[12:13]
	v_and_b32_e32 v9, 8, v8
	v_cmp_ne_u32_e64 s[18:19], 0, v9
	v_and_b32_e32 v9, 4, v8
	v_cmp_ne_u32_e64 s[16:17], 0, v9
	v_and_b32_e32 v9, 2, v8
	v_cmp_ne_u32_e64 s[12:13], 0, v9
	v_and_b32_e32 v9, 1, v8
	v_cmp_ne_u32_e64 s[8:9], 0, v9
	s_bcnt1_i32_b64 s7, s[18:19]
	s_bcnt1_i32_b64 s3, s[16:17]
	s_lshl1_add_u32 s7, s7, s3
	s_bcnt1_i32_b64 s3, s[12:13]
	s_lshl1_add_u32 s7, s7, s3
	s_bcnt1_i32_b64 s3, s[8:9]
	s_lshl1_add_u32 s7, s7, s3
	s_cmp_lt_u32 s7, s11
	s_cselect_b32 s4, s4, s6
	s_lshr_b32 s5, s5, 1
	s_cmp_lg_u32 s5, 0x80000
	s_cbranch_scc1 .Ltk2_a32
	s_mov_b32 s10, s4
	s_add_u32 s6, s4, 0x100000
	s_cbranch_scc1 .Ltk2_f32
	s_mov_b32 s5, 0
.Ltk2_b32:
	v_cmp_le_u32_e64 s[8:9], s6, v111
	v_cmp_le_u32_e64 s[12:13], s6, v113
	v_cmp_le_u32_e64 s[16:17], s6, v115
	v_cndmask_b32_e64 v8, 0, 1, s[8:9]
	v_cmp_le_u32_e64 s[8:9], s6, v117
	v_addc_co_u32_e64 v8, s[20:21], 0, v8, s[12:13]
	v_cmp_le_u32_e64 s[12:13], s6, v119
	v_addc_co_u32_e64 v8, s[20:21], 0, v8, s[16:17]
	v_cmp_le_u32_e64 s[16:17], s6, v121
	v_addc_co_u32_e64 v8, s[20:21], 0, v8, s[8:9]
	v_cmp_le_u32_e64 s[8:9], s6, v123
	v_addc_co_u32_e64 v8, s[20:21], 0, v8, s[12:13]
	v_cmp_le_u32_e64 s[12:13], s6, v124
	v_addc_co_u32_e64 v8, s[20:21], 0, v8, s[16:17]
	v_cmp_le_u32_e64 s[16:17], s6, v125
	v_addc_co_u32_e64 v8, s[20:21], 0, v8, s[8:9]
	v_cmp_le_u32_e64 s[8:9], s6, v126
	v_addc_co_u32_e64 v8, s[20:21], 0, v8, s[12:13]
	v_cmp_le_u32_e64 s[12:13], s6, v127
	v_addc_co_u32_e64 v8, s[20:21], 0, v8, s[16:17]
	v_cmp_le_u32_e64 s[16:17], s6, v128
	v_addc_co_u32_e64 v8, s[20:21], 0, v8, s[8:9]
	v_cmp_le_u32_e64 s[8:9], s6, v129
	v_addc_co_u32_e64 v8, s[20:21], 0, v8, s[12:13]
	v_cmp_le_u32_e64 s[12:13], s6, v130
	v_addc_co_u32_e64 v8, s[20:21], 0, v8, s[16:17]
	v_cmp_le_u32_e64 s[16:17], s6, v132
	v_addc_co_u32_e64 v8, s[20:21], 0, v8, s[8:9]
	v_cmp_le_u32_e64 s[8:9], s6, v133
	v_addc_co_u32_e64 v8, s[20:21], 0, v8, s[12:13]
	v_cmp_le_u32_e64 s[12:13], s6, v138
	v_addc_co_u32_e64 v8, s[20:21], 0, v8, s[16:17]
	v_cmp_le_u32_e64 s[16:17], s6, v139
	v_addc_co_u32_e64 v8, s[20:21], 0, v8, s[8:9]
	v_cmp_le_u32_e64 s[8:9], s6, v141
	v_addc_co_u32_e64 v8, s[20:21], 0, v8, s[12:13]
	v_cmp_le_u32_e64 s[12:13], s6, v143
	v_addc_co_u32_e64 v8, s[20:21], 0, v8, s[16:17]
	v_cmp_le_u32_e64 s[16:17], s6, v145
	v_addc_co_u32_e64 v8, s[20:21], 0, v8, s[8:9]
	v_cmp_le_u32_e64 s[8:9], s6, v147
	v_addc_co_u32_e64 v8, s[20:21], 0, v8, s[12:13]
	v_cmp_le_u32_e64 s[12:13], s6, v149
	v_addc_co_u32_e64 v8, s[20:21], 0, v8, s[16:17]
	v_cmp_le_u32_e64 s[16:17], s6, v151
	v_addc_co_u32_e64 v8, s[20:21], 0, v8, s[8:9]
	v_cmp_le_u32_e64 s[8:9], s6, v160
	v_addc_co_u32_e64 v8, s[20:21], 0, v8, s[12:13]
	v_cmp_le_u32_e64 s[12:13], s6, v163
	v_addc_co_u32_e64 v8, s[20:21], 0, v8, s[16:17]
	v_cmp_le_u32_e64 s[16:17], s6, v165
	v_addc_co_u32_e64 v8, s[20:21], 0, v8, s[8:9]
	v_cmp_le_u32_e64 s[8:9], s6, v166
	v_addc_co_u32_e64 v8, s[20:21], 0, v8, s[12:13]
	v_cmp_le_u32_e64 s[12:13], s6, v167
	v_addc_co_u32_e64 v8, s[20:21], 0, v8, s[16:17]
	v_cmp_le_u32_e64 s[16:17], s6, v168
	v_addc_co_u32_e64 v8, s[20:21], 0, v8, s[8:9]
	v_cmp_le_u32_e64 s[8:9], s6, v169
	v_addc_co_u32_e64 v8, s[20:21], 0, v8, s[12:13]
	v_cmp_le_u32_e64 s[12:13], s6, v6
	v_addc_co_u32_e64 v8, s[20:21], 0, v8, s[16:17]
	v_addc_co_u32_e64 v8, s[20:21], 0, v8, s[8:9]
	v_addc_co_u32_e64 v8, s[20:21], 0, v8, s[12:13]
	v_and_b32_e32 v9, 32, v8
	v_cmp_ne_u32_e64 s[0:1], 0, v9
	v_and_b32_e32 v9, 16, v8
	v_cmp_ne_u32_e64 s[22:23], 0, v9
	v_and_b32_e32 v9, 8, v8
	v_cmp_ne_u32_e64 s[18:19], 0, v9
	v_and_b32_e32 v9, 4, v8
	v_cmp_ne_u32_e64 s[16:17], 0, v9
	v_and_b32_e32 v9, 2, v8
	v_cmp_ne_u32_e64 s[12:13], 0, v9
	v_and_b32_e32 v9, 1, v8
	v_cmp_ne_u32_e64 s[8:9], 0, v9
	s_bcnt1_i32_b64 s7, s[0:1]
	s_bcnt1_i32_b64 s3, s[22:23]
	s_lshl1_add_u32 s7, s7, s3
	s_bcnt1_i32_b64 s3, s[18:19]
	s_lshl1_add_u32 s7, s7, s3
	s_bcnt1_i32_b64 s3, s[16:17]
	s_lshl1_add_u32 s7, s7, s3
	s_bcnt1_i32_b64 s3, s[12:13]
	s_lshl1_add_u32 s7, s7, s3
	s_bcnt1_i32_b64 s3, s[8:9]
	s_lshl1_add_u32 s7, s7, s3
	s_cmp_lg_u32 s5, 0
	s_cbranch_scc1 .Ltk2_c32
	s_cmpk_ge_u32 s7, 0x100
	s_cbranch_scc1 .Ltk2_f32
	s_mov_b32 s6, s10
	s_mov_b32 s5, 1
	s_branch .Ltk2_b32

.Ltk2_a28:
	s_or_b32 s6, s4, s5
	v_cmp_le_u32_e64 s[8:9], s6, v113
	v_cmp_le_u32_e64 s[12:13], s6, v121
	v_cmp_le_u32_e64 s[16:17], s6, v126
	v_cndmask_b32_e64 v8, 0, 1, s[8:9]
	v_cmp_le_u32_e64 s[8:9], s6, v130
	v_addc_co_u32_e64 v8, s[20:21], 0, v8, s[12:13]
	v_cmp_le_u32_e64 s[12:13], s6, v139
	v_addc_co_u32_e64 v8, s[20:21], 0, v8, s[16:17]
	v_cmp_le_u32_e64 s[16:17], s6, v147
	v_addc_co_u32_e64 v8, s[20:21], 0, v8, s[8:9]
	v_cmp_le_u32_e64 s[8:9], s6, v163
	v_addc_co_u32_e64 v8, s[20:21], 0, v8, s[12:13]
	v_addc_co_u32_e64 v8, s[20:21], 0, v8, s[16:17]
	v_addc_co_u32_e64 v8, s[20:21], 0, v8, s[8:9]
	v_and_b32_e32 v9, 4, v8
	v_cmp_ne_u32_e64 s[16:17], 0, v9
	v_and_b32_e32 v9, 2, v8
	v_cmp_ne_u32_e64 s[12:13], 0, v9
	v_and_b32_e32 v9, 1, v8
	v_cmp_ne_u32_e64 s[8:9], 0, v9
	s_bcnt1_i32_b64 s7, s[16:17]
	s_bcnt1_i32_b64 s3, s[12:13]
	s_lshl1_add_u32 s7, s7, s3
	s_bcnt1_i32_b64 s3, s[8:9]
	s_lshl1_add_u32 s7, s7, s3
	s_cmp_lt_u32 s7, s11
	s_cselect_b32 s4, s4, s6
	s_lshr_b32 s5, s5, 1
	s_cmp_lg_u32 s5, 0x80000
	s_cbranch_scc1 .Ltk2_a28
	s_mov_b32 s10, s4
	s_add_u32 s6, s4, 0x100000
	s_cbranch_scc1 .Ltk2_f28
	s_mov_b32 s5, 0
.Ltk2_b28:
	v_cmp_le_u32_e64 s[8:9], s6, v111
	v_cmp_le_u32_e64 s[12:13], s6, v113
	v_cmp_le_u32_e64 s[16:17], s6, v115
	v_cndmask_b32_e64 v8, 0, 1, s[8:9]
	v_cmp_le_u32_e64 s[8:9], s6, v117
	v_addc_co_u32_e64 v8, s[20:21], 0, v8, s[12:13]
	v_cmp_le_u32_e64 s[12:13], s6, v119
	v_addc_co_u32_e64 v8, s[20:21], 0, v8, s[16:17]
	v_cmp_le_u32_e64 s[16:17], s6, v121
	v_addc_co_u32_e64 v8, s[20:21], 0, v8, s[8:9]
	v_cmp_le_u32_e64 s[8:9], s6, v123
	v_addc_co_u32_e64 v8, s[20:21], 0, v8, s[12:13]
	v_cmp_le_u32_e64 s[12:13], s6, v124
	v_addc_co_u32_e64 v8, s[20:21], 0, v8, s[16:17]
	v_cmp_le_u32_e64 s[16:17], s6, v125
	v_addc_co_u32_e64 v8, s[20:21], 0, v8, s[8:9]
	v_cmp_le_u32_e64 s[8:9], s6, v126
	v_addc_co_u32_e64 v8, s[20:21], 0, v8, s[12:13]
	v_cmp_le_u32_e64 s[12:13], s6, v127
	v_addc_co_u32_e64 v8, s[20:21], 0, v8, s[16:17]
	v_cmp_le_u32_e64 s[16:17], s6, v128
	v_addc_co_u32_e64 v8, s[20:21], 0, v8, s[8:9]
	v_cmp_le_u32_e64 s[8:9], s6, v129
	v_addc_co_u32_e64 v8, s[20:21], 0, v8, s[12:13]
	v_cmp_le_u32_e64 s[12:13], s6, v130
	v_addc_co_u32_e64 v8, s[20:21], 0, v8, s[16:17]
	v_cmp_le_u32_e64 s[16:17], s6, v132
	v_addc_co_u32_e64 v8, s[20:21], 0, v8, s[8:9]
	v_cmp_le_u32_e64 s[8:9], s6, v133
	v_addc_co_u32_e64 v8, s[20:21], 0, v8, s[12:13]
	v_cmp_le_u32_e64 s[12:13], s6, v138
	v_addc_co_u32_e64 v8, s[20:21], 0, v8, s[16:17]
	v_cmp_le_u32_e64 s[16:17], s6, v139
	v_addc_co_u32_e64 v8, s[20:21], 0, v8, s[8:9]
	v_cmp_le_u32_e64 s[8:9], s6, v141
	v_addc_co_u32_e64 v8, s[20:21], 0, v8, s[12:13]
	v_cmp_le_u32_e64 s[12:13], s6, v143
	v_addc_co_u32_e64 v8, s[20:21], 0, v8, s[16:17]
	v_cmp_le_u32_e64 s[16:17], s6, v145
	v_addc_co_u32_e64 v8, s[20:21], 0, v8, s[8:9]
	v_cmp_le_u32_e64 s[8:9], s6, v147
	v_addc_co_u32_e64 v8, s[20:21], 0, v8, s[12:13]
	v_cmp_le_u32_e64 s[12:13], s6, v149
	v_addc_co_u32_e64 v8, s[20:21], 0, v8, s[16:17]
	v_cmp_le_u32_e64 s[16:17], s6, v151
	v_addc_co_u32_e64 v8, s[20:21], 0, v8, s[8:9]
	v_cmp_le_u32_e64 s[8:9], s6, v160
	v_addc_co_u32_e64 v8, s[20:21], 0, v8, s[12:13]
	v_cmp_le_u32_e64 s[12:13], s6, v163
	v_addc_co_u32_e64 v8, s[20:21], 0, v8, s[16:17]
	v_cmp_le_u32_e64 s[16:17], s6, v165
	v_addc_co_u32_e64 v8, s[20:21], 0, v8, s[8:9]
	v_cmp_le_u32_e64 s[8:9], s6, v166
	v_addc_co_u32_e64 v8, s[20:21], 0, v8, s[12:13]
	v_addc_co_u32_e64 v8, s[20:21], 0, v8, s[16:17]
	v_addc_co_u32_e64 v8, s[20:21], 0, v8, s[8:9]
	v_and_b32_e32 v9, 16, v8
	v_cmp_ne_u32_e64 s[22:23], 0, v9
	v_and_b32_e32 v9, 8, v8
	v_cmp_ne_u32_e64 s[18:19], 0, v9
	v_and_b32_e32 v9, 4, v8
	v_cmp_ne_u32_e64 s[16:17], 0, v9
	v_and_b32_e32 v9, 2, v8
	v_cmp_ne_u32_e64 s[12:13], 0, v9
	v_and_b32_e32 v9, 1, v8
	v_cmp_ne_u32_e64 s[8:9], 0, v9
	s_bcnt1_i32_b64 s7, s[22:23]
	s_bcnt1_i32_b64 s3, s[18:19]
	s_lshl1_add_u32 s7, s7, s3
	s_bcnt1_i32_b64 s3, s[16:17]
	s_lshl1_add_u32 s7, s7, s3
	s_bcnt1_i32_b64 s3, s[12:13]
	s_lshl1_add_u32 s7, s7, s3
	s_bcnt1_i32_b64 s3, s[8:9]
	s_lshl1_add_u32 s7, s7, s3
	s_cmp_lg_u32 s5, 0
	s_cbranch_scc1 .Ltk2_c28
	s_cmpk_ge_u32 s7, 0x100
	s_cbranch_scc1 .Ltk2_f28
	s_mov_b32 s6, s10
	s_mov_b32 s5, 1
	s_branch .Ltk2_b28

.Ltk2_a24:
	s_or_b32 s6, s4, s5
	v_cmp_le_u32_e64 s[8:9], s6, v113
	v_cmp_le_u32_e64 s[12:13], s6, v121
	v_cmp_le_u32_e64 s[16:17], s6, v126
	v_cndmask_b32_e64 v8, 0, 1, s[8:9]
	v_cmp_le_u32_e64 s[8:9], s6, v130
	v_addc_co_u32_e64 v8, s[20:21], 0, v8, s[12:13]
	v_cmp_le_u32_e64 s[12:13], s6, v139
	v_addc_co_u32_e64 v8, s[20:21], 0, v8, s[16:17]
	v_cmp_le_u32_e64 s[16:17], s6, v147
	v_addc_co_u32_e64 v8, s[20:21], 0, v8, s[8:9]
	v_addc_co_u32_e64 v8, s[20:21], 0, v8, s[12:13]
	v_addc_co_u32_e64 v8, s[20:21], 0, v8, s[16:17]
	v_and_b32_e32 v9, 4, v8
	v_cmp_ne_u32_e64 s[16:17], 0, v9
	v_and_b32_e32 v9, 2, v8
	v_cmp_ne_u32_e64 s[12:13], 0, v9
	v_and_b32_e32 v9, 1, v8
	v_cmp_ne_u32_e64 s[8:9], 0, v9
	s_bcnt1_i32_b64 s7, s[16:17]
	s_bcnt1_i32_b64 s3, s[12:13]
	s_lshl1_add_u32 s7, s7, s3
	s_bcnt1_i32_b64 s3, s[8:9]
	s_lshl1_add_u32 s7, s7, s3
	s_cmp_lt_u32 s7, s11
	s_cselect_b32 s4, s4, s6
	s_lshr_b32 s5, s5, 1
	s_cmp_lg_u32 s5, 0x80000
	s_cbranch_scc1 .Ltk2_a24
	s_mov_b32 s10, s4
	s_add_u32 s6, s4, 0x100000
	s_cbranch_scc1 .Ltk2_f24
	s_mov_b32 s5, 0
.Ltk2_b24:
	v_cmp_le_u32_e64 s[8:9], s6, v111
	v_cmp_le_u32_e64 s[12:13], s6, v113
	v_cmp_le_u32_e64 s[16:17], s6, v115
	v_cndmask_b32_e64 v8, 0, 1, s[8:9]
	v_cmp_le_u32_e64 s[8:9], s6, v117
	v_addc_co_u32_e64 v8, s[20:21], 0, v8, s[12:13]
	v_cmp_le_u32_e64 s[12:13], s6, v119
	v_addc_co_u32_e64 v8, s[20:21], 0, v8, s[16:17]
	v_cmp_le_u32_e64 s[16:17], s6, v121
	v_addc_co_u32_e64 v8, s[20:21], 0, v8, s[8:9]
	v_cmp_le_u32_e64 s[8:9], s6, v123
	v_addc_co_u32_e64 v8, s[20:21], 0, v8, s[12:13]
	v_cmp_le_u32_e64 s[12:13], s6, v124
	v_addc_co_u32_e64 v8, s[20:21], 0, v8, s[16:17]
	v_cmp_le_u32_e64 s[16:17], s6, v125
	v_addc_co_u32_e64 v8, s[20:21], 0, v8, s[8:9]
	v_cmp_le_u32_e64 s[8:9], s6, v126
	v_addc_co_u32_e64 v8, s[20:21], 0, v8, s[12:13]
	v_cmp_le_u32_e64 s[12:13], s6, v127
	v_addc_co_u32_e64 v8, s[20:21], 0, v8, s[16:17]
	v_cmp_le_u32_e64 s[16:17], s6, v128
	v_addc_co_u32_e64 v8, s[20:21], 0, v8, s[8:9]
	v_cmp_le_u32_e64 s[8:9], s6, v129
	v_addc_co_u32_e64 v8, s[20:21], 0, v8, s[12:13]
	v_cmp_le_u32_e64 s[12:13], s6, v130
	v_addc_co_u32_e64 v8, s[20:21], 0, v8, s[16:17]
	v_cmp_le_u32_e64 s[16:17], s6, v132
	v_addc_co_u32_e64 v8, s[20:21], 0, v8, s[8:9]
	v_cmp_le_u32_e64 s[8:9], s6, v133
	v_addc_co_u32_e64 v8, s[20:21], 0, v8, s[12:13]
	v_cmp_le_u32_e64 s[12:13], s6, v138
	v_addc_co_u32_e64 v8, s[20:21], 0, v8, s[16:17]
	v_cmp_le_u32_e64 s[16:17], s6, v139
	v_addc_co_u32_e64 v8, s[20:21], 0, v8, s[8:9]
	v_cmp_le_u32_e64 s[8:9], s6, v141
	v_addc_co_u32_e64 v8, s[20:21], 0, v8, s[12:13]
	v_cmp_le_u32_e64 s[12:13], s6, v143
	v_addc_co_u32_e64 v8, s[20:21], 0, v8, s[16:17]
	v_cmp_le_u32_e64 s[16:17], s6, v145
	v_addc_co_u32_e64 v8, s[20:21], 0, v8, s[8:9]
	v_cmp_le_u32_e64 s[8:9], s6, v147
	v_addc_co_u32_e64 v8, s[20:21], 0, v8, s[12:13]
	v_cmp_le_u32_e64 s[12:13], s6, v149
	v_addc_co_u32_e64 v8, s[20:21], 0, v8, s[16:17]
	v_cmp_le_u32_e64 s[16:17], s6, v151
	v_addc_co_u32_e64 v8, s[20:21], 0, v8, s[8:9]
	v_addc_co_u32_e64 v8, s[20:21], 0, v8, s[12:13]
	v_addc_co_u32_e64 v8, s[20:21], 0, v8, s[16:17]
	v_and_b32_e32 v9, 16, v8
	v_cmp_ne_u32_e64 s[22:23], 0, v9
	v_and_b32_e32 v9, 8, v8
	v_cmp_ne_u32_e64 s[18:19], 0, v9
	v_and_b32_e32 v9, 4, v8
	v_cmp_ne_u32_e64 s[16:17], 0, v9
	v_and_b32_e32 v9, 2, v8
	v_cmp_ne_u32_e64 s[12:13], 0, v9
	v_and_b32_e32 v9, 1, v8
	v_cmp_ne_u32_e64 s[8:9], 0, v9
	s_bcnt1_i32_b64 s7, s[22:23]
	s_bcnt1_i32_b64 s3, s[18:19]
	s_lshl1_add_u32 s7, s7, s3
	s_bcnt1_i32_b64 s3, s[16:17]
	s_lshl1_add_u32 s7, s7, s3
	s_bcnt1_i32_b64 s3, s[12:13]
	s_lshl1_add_u32 s7, s7, s3
	s_bcnt1_i32_b64 s3, s[8:9]
	s_lshl1_add_u32 s7, s7, s3
	s_cmp_lg_u32 s5, 0
	s_cbranch_scc1 .Ltk2_c24
	s_cmpk_ge_u32 s7, 0x100
	s_cbranch_scc1 .Ltk2_f24
	s_mov_b32 s6, s10
	s_mov_b32 s5, 1
	s_branch .Ltk2_b24

.Ltk2_a20:
	s_or_b32 s6, s4, s5
	v_cmp_le_u32_e64 s[8:9], s6, v113
	v_cmp_le_u32_e64 s[12:13], s6, v121
	v_cmp_le_u32_e64 s[16:17], s6, v126
	v_cndmask_b32_e64 v8, 0, 1, s[8:9]
	v_cmp_le_u32_e64 s[8:9], s6, v130
	v_addc_co_u32_e64 v8, s[20:21], 0, v8, s[12:13]
	v_cmp_le_u32_e64 s[12:13], s6, v139
	v_addc_co_u32_e64 v8, s[20:21], 0, v8, s[16:17]
	v_addc_co_u32_e64 v8, s[20:21], 0, v8, s[8:9]
	v_addc_co_u32_e64 v8, s[20:21], 0, v8, s[12:13]
	v_and_b32_e32 v9, 4, v8
	v_cmp_ne_u32_e64 s[16:17], 0, v9
	v_and_b32_e32 v9, 2, v8
	v_cmp_ne_u32_e64 s[12:13], 0, v9
	v_and_b32_e32 v9, 1, v8
	v_cmp_ne_u32_e64 s[8:9], 0, v9
	s_bcnt1_i32_b64 s7, s[16:17]
	s_bcnt1_i32_b64 s3, s[12:13]
	s_lshl1_add_u32 s7, s7, s3
	s_bcnt1_i32_b64 s3, s[8:9]
	s_lshl1_add_u32 s7, s7, s3
	s_cmp_lt_u32 s7, s11
	s_cselect_b32 s4, s4, s6
	s_lshr_b32 s5, s5, 1
	s_cmp_lg_u32 s5, 0x80000
	s_cbranch_scc1 .Ltk2_a20
	s_mov_b32 s10, s4
	s_add_u32 s6, s4, 0x100000
	s_cbranch_scc1 .Ltk2_f20
	s_mov_b32 s5, 0
.Ltk2_b20:
	v_cmp_le_u32_e64 s[8:9], s6, v111
	v_cmp_le_u32_e64 s[12:13], s6, v113
	v_cmp_le_u32_e64 s[16:17], s6, v115
	v_cndmask_b32_e64 v8, 0, 1, s[8:9]
	v_cmp_le_u32_e64 s[8:9], s6, v117
	v_addc_co_u32_e64 v8, s[20:21], 0, v8, s[12:13]
	v_cmp_le_u32_e64 s[12:13], s6, v119
	v_addc_co_u32_e64 v8, s[20:21], 0, v8, s[16:17]
	v_cmp_le_u32_e64 s[16:17], s6, v121
	v_addc_co_u32_e64 v8, s[20:21], 0, v8, s[8:9]
	v_cmp_le_u32_e64 s[8:9], s6, v123
	v_addc_co_u32_e64 v8, s[20:21], 0, v8, s[12:13]
	v_cmp_le_u32_e64 s[12:13], s6, v124
	v_addc_co_u32_e64 v8, s[20:21], 0, v8, s[16:17]
	v_cmp_le_u32_e64 s[16:17], s6, v125
	v_addc_co_u32_e64 v8, s[20:21], 0, v8, s[8:9]
	v_cmp_le_u32_e64 s[8:9], s6, v126
	v_addc_co_u32_e64 v8, s[20:21], 0, v8, s[12:13]
	v_cmp_le_u32_e64 s[12:13], s6, v127
	v_addc_co_u32_e64 v8, s[20:21], 0, v8, s[16:17]
	v_cmp_le_u32_e64 s[16:17], s6, v128
	v_addc_co_u32_e64 v8, s[20:21], 0, v8, s[8:9]
	v_cmp_le_u32_e64 s[8:9], s6, v129
	v_addc_co_u32_e64 v8, s[20:21], 0, v8, s[12:13]
	v_cmp_le_u32_e64 s[12:13], s6, v130
	v_addc_co_u32_e64 v8, s[20:21], 0, v8, s[16:17]
	v_cmp_le_u32_e64 s[16:17], s6, v132
	v_addc_co_u32_e64 v8, s[20:21], 0, v8, s[8:9]
	v_cmp_le_u32_e64 s[8:9], s6, v133
	v_addc_co_u32_e64 v8, s[20:21], 0, v8, s[12:13]
	v_cmp_le_u32_e64 s[12:13], s6, v138
	v_addc_co_u32_e64 v8, s[20:21], 0, v8, s[16:17]
	v_cmp_le_u32_e64 s[16:17], s6, v139
	v_addc_co_u32_e64 v8, s[20:21], 0, v8, s[8:9]
	v_cmp_le_u32_e64 s[8:9], s6, v141
	v_addc_co_u32_e64 v8, s[20:21], 0, v8, s[12:13]
	v_cmp_le_u32_e64 s[12:13], s6, v143
	v_addc_co_u32_e64 v8, s[20:21], 0, v8, s[16:17]
	v_addc_co_u32_e64 v8, s[20:21], 0, v8, s[8:9]
	v_addc_co_u32_e64 v8, s[20:21], 0, v8, s[12:13]
	v_and_b32_e32 v9, 16, v8
	v_cmp_ne_u32_e64 s[22:23], 0, v9
	v_and_b32_e32 v9, 8, v8
	v_cmp_ne_u32_e64 s[18:19], 0, v9
	v_and_b32_e32 v9, 4, v8
	v_cmp_ne_u32_e64 s[16:17], 0, v9
	v_and_b32_e32 v9, 2, v8
	v_cmp_ne_u32_e64 s[12:13], 0, v9
	v_and_b32_e32 v9, 1, v8
	v_cmp_ne_u32_e64 s[8:9], 0, v9
	s_bcnt1_i32_b64 s7, s[22:23]
	s_bcnt1_i32_b64 s3, s[18:19]
	s_lshl1_add_u32 s7, s7, s3
	s_bcnt1_i32_b64 s3, s[16:17]
	s_lshl1_add_u32 s7, s7, s3
	s_bcnt1_i32_b64 s3, s[12:13]
	s_lshl1_add_u32 s7, s7, s3
	s_bcnt1_i32_b64 s3, s[8:9]
	s_lshl1_add_u32 s7, s7, s3
	s_cmp_lg_u32 s5, 0
	s_cbranch_scc1 .Ltk2_c20
	s_cmpk_ge_u32 s7, 0x100
	s_cbranch_scc1 .Ltk2_f20
	s_mov_b32 s6, s10
	s_mov_b32 s5, 1
	s_branch .Ltk2_b20

.Ltk3_a32:
	s_or_b32 s6, s4, s5
	v_cmp_le_u32_e64 s[8:9], s6, v94
	v_cmp_le_u32_e64 s[12:13], s6, v98
	v_cmp_le_u32_e64 s[16:17], s6, v102
	v_cndmask_b32_e64 v8, 0, 1, s[8:9]
	v_cmp_le_u32_e64 s[8:9], s6, v106
	v_addc_co_u32_e64 v8, s[20:21], 0, v8, s[12:13]
	v_cmp_le_u32_e64 s[12:13], s6, v110
	v_addc_co_u32_e64 v8, s[20:21], 0, v8, s[16:17]
	v_cmp_le_u32_e64 s[16:17], s6, v118
	v_addc_co_u32_e64 v8, s[20:21], 0, v8, s[8:9]
	v_cmp_le_u32_e64 s[8:9], s6, v90
	v_addc_co_u32_e64 v8, s[20:21], 0, v8, s[12:13]
	v_cmp_le_u32_e64 s[12:13], s6, v136
	v_addc_co_u32_e64 v8, s[20:21], 0, v8, s[16:17]
	v_addc_co_u32_e64 v8, s[20:21], 0, v8, s[8:9]
	v_addc_co_u32_e64 v8, s[20:21], 0, v8, s[12:13]
	v_and_b32_e32 v9, 8, v8
	v_cmp_ne_u32_e64 s[18:19], 0, v9
	v_and_b32_e32 v9, 4, v8
	v_cmp_ne_u32_e64 s[16:17], 0, v9
	v_and_b32_e32 v9, 2, v8
	v_cmp_ne_u32_e64 s[12:13], 0, v9
	v_and_b32_e32 v9, 1, v8
	v_cmp_ne_u32_e64 s[8:9], 0, v9
	s_bcnt1_i32_b64 s7, s[18:19]
	s_bcnt1_i32_b64 s3, s[16:17]
	s_lshl1_add_u32 s7, s7, s3
	s_bcnt1_i32_b64 s3, s[12:13]
	s_lshl1_add_u32 s7, s7, s3
	s_bcnt1_i32_b64 s3, s[8:9]
	s_lshl1_add_u32 s7, s7, s3
	s_cmp_lt_u32 s7, s11
	s_cselect_b32 s4, s4, s6
	s_lshr_b32 s5, s5, 1
	s_cmp_lg_u32 s5, 0x80000
	s_cbranch_scc1 .Ltk3_a32
	s_mov_b32 s10, s4
	s_add_u32 s6, s4, 0x100000
	s_cbranch_scc1 .Ltk3_f32
	s_mov_b32 s5, 0
.Ltk3_b32:
	v_cmp_le_u32_e64 s[8:9], s6, v93
	v_cmp_le_u32_e64 s[12:13], s6, v94
	v_cmp_le_u32_e64 s[16:17], s6, v95
	v_cndmask_b32_e64 v8, 0, 1, s[8:9]
	v_cmp_le_u32_e64 s[8:9], s6, v96
	v_addc_co_u32_e64 v8, s[20:21], 0, v8, s[12:13]
	v_cmp_le_u32_e64 s[12:13], s6, v97
	v_addc_co_u32_e64 v8, s[20:21], 0, v8, s[16:17]
	v_cmp_le_u32_e64 s[16:17], s6, v98
	v_addc_co_u32_e64 v8, s[20:21], 0, v8, s[8:9]
	v_cmp_le_u32_e64 s[8:9], s6, v99
	v_addc_co_u32_e64 v8, s[20:21], 0, v8, s[12:13]
	v_cmp_le_u32_e64 s[12:13], s6, v100
	v_addc_co_u32_e64 v8, s[20:21], 0, v8, s[16:17]
	v_cmp_le_u32_e64 s[16:17], s6, v101
	v_addc_co_u32_e64 v8, s[20:21], 0, v8, s[8:9]
	v_cmp_le_u32_e64 s[8:9], s6, v102
	v_addc_co_u32_e64 v8, s[20:21], 0, v8, s[12:13]
	v_cmp_le_u32_e64 s[12:13], s6, v103
	v_addc_co_u32_e64 v8, s[20:21], 0, v8, s[16:17]
	v_cmp_le_u32_e64 s[16:17], s6, v104
	v_addc_co_u32_e64 v8, s[20:21], 0, v8, s[8:9]
	v_cmp_le_u32_e64 s[8:9], s6, v105
	v_addc_co_u32_e64 v8, s[20:21], 0, v8, s[12:13]
	v_cmp_le_u32_e64 s[12:13], s6, v106
	v_addc_co_u32_e64 v8, s[20:21], 0, v8, s[16:17]
	v_cmp_le_u32_e64 s[16:17], s6, v107
	v_addc_co_u32_e64 v8, s[20:21], 0, v8, s[8:9]
	v_cmp_le_u32_e64 s[8:9], s6, v108
	v_addc_co_u32_e64 v8, s[20:21], 0, v8, s[12:13]
	v_cmp_le_u32_e64 s[12:13], s6, v109
	v_addc_co_u32_e64 v8, s[20:21], 0, v8, s[16:17]
	v_cmp_le_u32_e64 s[16:17], s6, v110
	v_addc_co_u32_e64 v8, s[20:21], 0, v8, s[8:9]
	v_cmp_le_u32_e64 s[8:9], s6, v112
	v_addc_co_u32_e64 v8, s[20:21], 0, v8, s[12:13]
	v_cmp_le_u32_e64 s[12:13], s6, v114
	v_addc_co_u32_e64 v8, s[20:21], 0, v8, s[16:17]
	v_cmp_le_u32_e64 s[16:17], s6, v116
	v_addc_co_u32_e64 v8, s[20:21], 0, v8, s[8:9]
	v_cmp_le_u32_e64 s[8:9], s6, v118
	v_addc_co_u32_e64 v8, s[20:21], 0, v8, s[12:13]
	v_cmp_le_u32_e64 s[12:13], s6, v120
	v_addc_co_u32_e64 v8, s[20:21], 0, v8, s[16:17]
	v_cmp_le_u32_e64 s[16:17], s6, v122
	v_addc_co_u32_e64 v8, s[20:21], 0, v8, s[8:9]
	v_cmp_le_u32_e64 s[8:9], s6, v131
	v_addc_co_u32_e64 v8, s[20:21], 0, v8, s[12:13]
	v_cmp_le_u32_e64 s[12:13], s6, v90
	v_addc_co_u32_e64 v8, s[20:21], 0, v8, s[16:17]
	v_cmp_le_u32_e64 s[16:17], s6, v91
	v_addc_co_u32_e64 v8, s[20:21], 0, v8, s[8:9]
	v_cmp_le_u32_e64 s[8:9], s6, v134
	v_addc_co_u32_e64 v8, s[20:21], 0, v8, s[12:13]
	v_cmp_le_u32_e64 s[12:13], s6, v135
	v_addc_co_u32_e64 v8, s[20:21], 0, v8, s[16:17]
	v_cmp_le_u32_e64 s[16:17], s6, v136
	v_addc_co_u32_e64 v8, s[20:21], 0, v8, s[8:9]
	v_cmp_le_u32_e64 s[8:9], s6, v137
	v_addc_co_u32_e64 v8, s[20:21], 0, v8, s[12:13]
	v_cmp_le_u32_e64 s[12:13], s6, v4
	v_addc_co_u32_e64 v8, s[20:21], 0, v8, s[16:17]
	v_addc_co_u32_e64 v8, s[20:21], 0, v8, s[8:9]
	v_addc_co_u32_e64 v8, s[20:21], 0, v8, s[12:13]
	v_and_b32_e32 v9, 32, v8
	v_cmp_ne_u32_e64 s[0:1], 0, v9
	v_and_b32_e32 v9, 16, v8
	v_cmp_ne_u32_e64 s[22:23], 0, v9
	v_and_b32_e32 v9, 8, v8
	v_cmp_ne_u32_e64 s[18:19], 0, v9
	v_and_b32_e32 v9, 4, v8
	v_cmp_ne_u32_e64 s[16:17], 0, v9
	v_and_b32_e32 v9, 2, v8
	v_cmp_ne_u32_e64 s[12:13], 0, v9
	v_and_b32_e32 v9, 1, v8
	v_cmp_ne_u32_e64 s[8:9], 0, v9
	s_bcnt1_i32_b64 s7, s[0:1]
	s_bcnt1_i32_b64 s3, s[22:23]
	s_lshl1_add_u32 s7, s7, s3
	s_bcnt1_i32_b64 s3, s[18:19]
	s_lshl1_add_u32 s7, s7, s3
	s_bcnt1_i32_b64 s3, s[16:17]
	s_lshl1_add_u32 s7, s7, s3
	s_bcnt1_i32_b64 s3, s[12:13]
	s_lshl1_add_u32 s7, s7, s3
	s_bcnt1_i32_b64 s3, s[8:9]
	s_lshl1_add_u32 s7, s7, s3
	s_cmp_lg_u32 s5, 0
	s_cbranch_scc1 .Ltk3_c32
	s_cmpk_ge_u32 s7, 0x100
	s_cbranch_scc1 .Ltk3_f32
	s_mov_b32 s6, s10
	s_mov_b32 s5, 1
	s_branch .Ltk3_b32

.Ltk3_a28:
	s_or_b32 s6, s4, s5
	v_cmp_le_u32_e64 s[8:9], s6, v94
	v_cmp_le_u32_e64 s[12:13], s6, v98
	v_cmp_le_u32_e64 s[16:17], s6, v102
	v_cndmask_b32_e64 v8, 0, 1, s[8:9]
	v_cmp_le_u32_e64 s[8:9], s6, v106
	v_addc_co_u32_e64 v8, s[20:21], 0, v8, s[12:13]
	v_cmp_le_u32_e64 s[12:13], s6, v110
	v_addc_co_u32_e64 v8, s[20:21], 0, v8, s[16:17]
	v_cmp_le_u32_e64 s[16:17], s6, v118
	v_addc_co_u32_e64 v8, s[20:21], 0, v8, s[8:9]
	v_cmp_le_u32_e64 s[8:9], s6, v90
	v_addc_co_u32_e64 v8, s[20:21], 0, v8, s[12:13]
	v_addc_co_u32_e64 v8, s[20:21], 0, v8, s[16:17]
	v_addc_co_u32_e64 v8, s[20:21], 0, v8, s[8:9]
	v_and_b32_e32 v9, 4, v8
	v_cmp_ne_u32_e64 s[16:17], 0, v9
	v_and_b32_e32 v9, 2, v8
	v_cmp_ne_u32_e64 s[12:13], 0, v9
	v_and_b32_e32 v9, 1, v8
	v_cmp_ne_u32_e64 s[8:9], 0, v9
	s_bcnt1_i32_b64 s7, s[16:17]
	s_bcnt1_i32_b64 s3, s[12:13]
	s_lshl1_add_u32 s7, s7, s3
	s_bcnt1_i32_b64 s3, s[8:9]
	s_lshl1_add_u32 s7, s7, s3
	s_cmp_lt_u32 s7, s11
	s_cselect_b32 s4, s4, s6
	s_lshr_b32 s5, s5, 1
	s_cmp_lg_u32 s5, 0x80000
	s_cbranch_scc1 .Ltk3_a28
	s_mov_b32 s10, s4
	s_add_u32 s6, s4, 0x100000
	s_cbranch_scc1 .Ltk3_f28
	s_mov_b32 s5, 0
.Ltk3_b28:
	v_cmp_le_u32_e64 s[8:9], s6, v93
	v_cmp_le_u32_e64 s[12:13], s6, v94
	v_cmp_le_u32_e64 s[16:17], s6, v95
	v_cndmask_b32_e64 v8, 0, 1, s[8:9]
	v_cmp_le_u32_e64 s[8:9], s6, v96
	v_addc_co_u32_e64 v8, s[20:21], 0, v8, s[12:13]
	v_cmp_le_u32_e64 s[12:13], s6, v97
	v_addc_co_u32_e64 v8, s[20:21], 0, v8, s[16:17]
	v_cmp_le_u32_e64 s[16:17], s6, v98
	v_addc_co_u32_e64 v8, s[20:21], 0, v8, s[8:9]
	v_cmp_le_u32_e64 s[8:9], s6, v99
	v_addc_co_u32_e64 v8, s[20:21], 0, v8, s[12:13]
	v_cmp_le_u32_e64 s[12:13], s6, v100
	v_addc_co_u32_e64 v8, s[20:21], 0, v8, s[16:17]
	v_cmp_le_u32_e64 s[16:17], s6, v101
	v_addc_co_u32_e64 v8, s[20:21], 0, v8, s[8:9]
	v_cmp_le_u32_e64 s[8:9], s6, v102
	v_addc_co_u32_e64 v8, s[20:21], 0, v8, s[12:13]
	v_cmp_le_u32_e64 s[12:13], s6, v103
	v_addc_co_u32_e64 v8, s[20:21], 0, v8, s[16:17]
	v_cmp_le_u32_e64 s[16:17], s6, v104
	v_addc_co_u32_e64 v8, s[20:21], 0, v8, s[8:9]
	v_cmp_le_u32_e64 s[8:9], s6, v105
	v_addc_co_u32_e64 v8, s[20:21], 0, v8, s[12:13]
	v_cmp_le_u32_e64 s[12:13], s6, v106
	v_addc_co_u32_e64 v8, s[20:21], 0, v8, s[16:17]
	v_cmp_le_u32_e64 s[16:17], s6, v107
	v_addc_co_u32_e64 v8, s[20:21], 0, v8, s[8:9]
	v_cmp_le_u32_e64 s[8:9], s6, v108
	v_addc_co_u32_e64 v8, s[20:21], 0, v8, s[12:13]
	v_cmp_le_u32_e64 s[12:13], s6, v109
	v_addc_co_u32_e64 v8, s[20:21], 0, v8, s[16:17]
	v_cmp_le_u32_e64 s[16:17], s6, v110
	v_addc_co_u32_e64 v8, s[20:21], 0, v8, s[8:9]
	v_cmp_le_u32_e64 s[8:9], s6, v112
	v_addc_co_u32_e64 v8, s[20:21], 0, v8, s[12:13]
	v_cmp_le_u32_e64 s[12:13], s6, v114
	v_addc_co_u32_e64 v8, s[20:21], 0, v8, s[16:17]
	v_cmp_le_u32_e64 s[16:17], s6, v116
	v_addc_co_u32_e64 v8, s[20:21], 0, v8, s[8:9]
	v_cmp_le_u32_e64 s[8:9], s6, v118
	v_addc_co_u32_e64 v8, s[20:21], 0, v8, s[12:13]
	v_cmp_le_u32_e64 s[12:13], s6, v120
	v_addc_co_u32_e64 v8, s[20:21], 0, v8, s[16:17]
	v_cmp_le_u32_e64 s[16:17], s6, v122
	v_addc_co_u32_e64 v8, s[20:21], 0, v8, s[8:9]
	v_cmp_le_u32_e64 s[8:9], s6, v131
	v_addc_co_u32_e64 v8, s[20:21], 0, v8, s[12:13]
	v_cmp_le_u32_e64 s[12:13], s6, v90
	v_addc_co_u32_e64 v8, s[20:21], 0, v8, s[16:17]
	v_cmp_le_u32_e64 s[16:17], s6, v91
	v_addc_co_u32_e64 v8, s[20:21], 0, v8, s[8:9]
	v_cmp_le_u32_e64 s[8:9], s6, v134
	v_addc_co_u32_e64 v8, s[20:21], 0, v8, s[12:13]
	v_addc_co_u32_e64 v8, s[20:21], 0, v8, s[16:17]
	v_addc_co_u32_e64 v8, s[20:21], 0, v8, s[8:9]
	v_and_b32_e32 v9, 16, v8
	v_cmp_ne_u32_e64 s[22:23], 0, v9
	v_and_b32_e32 v9, 8, v8
	v_cmp_ne_u32_e64 s[18:19], 0, v9
	v_and_b32_e32 v9, 4, v8
	v_cmp_ne_u32_e64 s[16:17], 0, v9
	v_and_b32_e32 v9, 2, v8
	v_cmp_ne_u32_e64 s[12:13], 0, v9
	v_and_b32_e32 v9, 1, v8
	v_cmp_ne_u32_e64 s[8:9], 0, v9
	s_bcnt1_i32_b64 s7, s[22:23]
	s_bcnt1_i32_b64 s3, s[18:19]
	s_lshl1_add_u32 s7, s7, s3
	s_bcnt1_i32_b64 s3, s[16:17]
	s_lshl1_add_u32 s7, s7, s3
	s_bcnt1_i32_b64 s3, s[12:13]
	s_lshl1_add_u32 s7, s7, s3
	s_bcnt1_i32_b64 s3, s[8:9]
	s_lshl1_add_u32 s7, s7, s3
	s_cmp_lg_u32 s5, 0
	s_cbranch_scc1 .Ltk3_c28
	s_cmpk_ge_u32 s7, 0x100
	s_cbranch_scc1 .Ltk3_f28
	s_mov_b32 s6, s10
	s_mov_b32 s5, 1
	s_branch .Ltk3_b28

.Ltk3_a24:
	s_or_b32 s6, s4, s5
	v_cmp_le_u32_e64 s[8:9], s6, v94
	v_cmp_le_u32_e64 s[12:13], s6, v98
	v_cmp_le_u32_e64 s[16:17], s6, v102
	v_cndmask_b32_e64 v8, 0, 1, s[8:9]
	v_cmp_le_u32_e64 s[8:9], s6, v106
	v_addc_co_u32_e64 v8, s[20:21], 0, v8, s[12:13]
	v_cmp_le_u32_e64 s[12:13], s6, v110
	v_addc_co_u32_e64 v8, s[20:21], 0, v8, s[16:17]
	v_cmp_le_u32_e64 s[16:17], s6, v118
	v_addc_co_u32_e64 v8, s[20:21], 0, v8, s[8:9]
	v_addc_co_u32_e64 v8, s[20:21], 0, v8, s[12:13]
	v_addc_co_u32_e64 v8, s[20:21], 0, v8, s[16:17]
	v_and_b32_e32 v9, 4, v8
	v_cmp_ne_u32_e64 s[16:17], 0, v9
	v_and_b32_e32 v9, 2, v8
	v_cmp_ne_u32_e64 s[12:13], 0, v9
	v_and_b32_e32 v9, 1, v8
	v_cmp_ne_u32_e64 s[8:9], 0, v9
	s_bcnt1_i32_b64 s7, s[16:17]
	s_bcnt1_i32_b64 s3, s[12:13]
	s_lshl1_add_u32 s7, s7, s3
	s_bcnt1_i32_b64 s3, s[8:9]
	s_lshl1_add_u32 s7, s7, s3
	s_cmp_lt_u32 s7, s11
	s_cselect_b32 s4, s4, s6
	s_lshr_b32 s5, s5, 1
	s_cmp_lg_u32 s5, 0x80000
	s_cbranch_scc1 .Ltk3_a24
	s_mov_b32 s10, s4
	s_add_u32 s6, s4, 0x100000
	s_cbranch_scc1 .Ltk3_f24
	s_mov_b32 s5, 0
.Ltk3_b24:
	v_cmp_le_u32_e64 s[8:9], s6, v93
	v_cmp_le_u32_e64 s[12:13], s6, v94
	v_cmp_le_u32_e64 s[16:17], s6, v95
	v_cndmask_b32_e64 v8, 0, 1, s[8:9]
	v_cmp_le_u32_e64 s[8:9], s6, v96
	v_addc_co_u32_e64 v8, s[20:21], 0, v8, s[12:13]
	v_cmp_le_u32_e64 s[12:13], s6, v97
	v_addc_co_u32_e64 v8, s[20:21], 0, v8, s[16:17]
	v_cmp_le_u32_e64 s[16:17], s6, v98
	v_addc_co_u32_e64 v8, s[20:21], 0, v8, s[8:9]
	v_cmp_le_u32_e64 s[8:9], s6, v99
	v_addc_co_u32_e64 v8, s[20:21], 0, v8, s[12:13]
	v_cmp_le_u32_e64 s[12:13], s6, v100
	v_addc_co_u32_e64 v8, s[20:21], 0, v8, s[16:17]
	v_cmp_le_u32_e64 s[16:17], s6, v101
	v_addc_co_u32_e64 v8, s[20:21], 0, v8, s[8:9]
	v_cmp_le_u32_e64 s[8:9], s6, v102
	v_addc_co_u32_e64 v8, s[20:21], 0, v8, s[12:13]
	v_cmp_le_u32_e64 s[12:13], s6, v103
	v_addc_co_u32_e64 v8, s[20:21], 0, v8, s[16:17]
	v_cmp_le_u32_e64 s[16:17], s6, v104
	v_addc_co_u32_e64 v8, s[20:21], 0, v8, s[8:9]
	v_cmp_le_u32_e64 s[8:9], s6, v105
	v_addc_co_u32_e64 v8, s[20:21], 0, v8, s[12:13]
	v_cmp_le_u32_e64 s[12:13], s6, v106
	v_addc_co_u32_e64 v8, s[20:21], 0, v8, s[16:17]
	v_cmp_le_u32_e64 s[16:17], s6, v107
	v_addc_co_u32_e64 v8, s[20:21], 0, v8, s[8:9]
	v_cmp_le_u32_e64 s[8:9], s6, v108
	v_addc_co_u32_e64 v8, s[20:21], 0, v8, s[12:13]
	v_cmp_le_u32_e64 s[12:13], s6, v109
	v_addc_co_u32_e64 v8, s[20:21], 0, v8, s[16:17]
	v_cmp_le_u32_e64 s[16:17], s6, v110
	v_addc_co_u32_e64 v8, s[20:21], 0, v8, s[8:9]
	v_cmp_le_u32_e64 s[8:9], s6, v112
	v_addc_co_u32_e64 v8, s[20:21], 0, v8, s[12:13]
	v_cmp_le_u32_e64 s[12:13], s6, v114
	v_addc_co_u32_e64 v8, s[20:21], 0, v8, s[16:17]
	v_cmp_le_u32_e64 s[16:17], s6, v116
	v_addc_co_u32_e64 v8, s[20:21], 0, v8, s[8:9]
	v_cmp_le_u32_e64 s[8:9], s6, v118
	v_addc_co_u32_e64 v8, s[20:21], 0, v8, s[12:13]
	v_cmp_le_u32_e64 s[12:13], s6, v120
	v_addc_co_u32_e64 v8, s[20:21], 0, v8, s[16:17]
	v_cmp_le_u32_e64 s[16:17], s6, v122
	v_addc_co_u32_e64 v8, s[20:21], 0, v8, s[8:9]
	v_addc_co_u32_e64 v8, s[20:21], 0, v8, s[12:13]
	v_addc_co_u32_e64 v8, s[20:21], 0, v8, s[16:17]
	v_and_b32_e32 v9, 16, v8
	v_cmp_ne_u32_e64 s[22:23], 0, v9
	v_and_b32_e32 v9, 8, v8
	v_cmp_ne_u32_e64 s[18:19], 0, v9
	v_and_b32_e32 v9, 4, v8
	v_cmp_ne_u32_e64 s[16:17], 0, v9
	v_and_b32_e32 v9, 2, v8
	v_cmp_ne_u32_e64 s[12:13], 0, v9
	v_and_b32_e32 v9, 1, v8
	v_cmp_ne_u32_e64 s[8:9], 0, v9
	s_bcnt1_i32_b64 s7, s[22:23]
	s_bcnt1_i32_b64 s3, s[18:19]
	s_lshl1_add_u32 s7, s7, s3
	s_bcnt1_i32_b64 s3, s[16:17]
	s_lshl1_add_u32 s7, s7, s3
	s_bcnt1_i32_b64 s3, s[12:13]
	s_lshl1_add_u32 s7, s7, s3
	s_bcnt1_i32_b64 s3, s[8:9]
	s_lshl1_add_u32 s7, s7, s3
	s_cmp_lg_u32 s5, 0
	s_cbranch_scc1 .Ltk3_c24
	s_cmpk_ge_u32 s7, 0x100
	s_cbranch_scc1 .Ltk3_f24
	s_mov_b32 s6, s10
	s_mov_b32 s5, 1
	s_branch .Ltk3_b24

.Ltk3_a20:
	s_or_b32 s6, s4, s5
	v_cmp_le_u32_e64 s[8:9], s6, v94
	v_cmp_le_u32_e64 s[12:13], s6, v98
	v_cmp_le_u32_e64 s[16:17], s6, v102
	v_cndmask_b32_e64 v8, 0, 1, s[8:9]
	v_cmp_le_u32_e64 s[8:9], s6, v106
	v_addc_co_u32_e64 v8, s[20:21], 0, v8, s[12:13]
	v_cmp_le_u32_e64 s[12:13], s6, v110
	v_addc_co_u32_e64 v8, s[20:21], 0, v8, s[16:17]
	v_addc_co_u32_e64 v8, s[20:21], 0, v8, s[8:9]
	v_addc_co_u32_e64 v8, s[20:21], 0, v8, s[12:13]
	v_and_b32_e32 v9, 4, v8
	v_cmp_ne_u32_e64 s[16:17], 0, v9
	v_and_b32_e32 v9, 2, v8
	v_cmp_ne_u32_e64 s[12:13], 0, v9
	v_and_b32_e32 v9, 1, v8
	v_cmp_ne_u32_e64 s[8:9], 0, v9
	s_bcnt1_i32_b64 s7, s[16:17]
	s_bcnt1_i32_b64 s3, s[12:13]
	s_lshl1_add_u32 s7, s7, s3
	s_bcnt1_i32_b64 s3, s[8:9]
	s_lshl1_add_u32 s7, s7, s3
	s_cmp_lt_u32 s7, s11
	s_cselect_b32 s4, s4, s6
	s_lshr_b32 s5, s5, 1
	s_cmp_lg_u32 s5, 0x80000
	s_cbranch_scc1 .Ltk3_a20
	s_mov_b32 s10, s4
	s_add_u32 s6, s4, 0x100000
	s_cbranch_scc1 .Ltk3_f20
	s_mov_b32 s5, 0
.Ltk3_b20:
	v_cmp_le_u32_e64 s[8:9], s6, v93
	v_cmp_le_u32_e64 s[12:13], s6, v94
	v_cmp_le_u32_e64 s[16:17], s6, v95
	v_cndmask_b32_e64 v8, 0, 1, s[8:9]
	v_cmp_le_u32_e64 s[8:9], s6, v96
	v_addc_co_u32_e64 v8, s[20:21], 0, v8, s[12:13]
	v_cmp_le_u32_e64 s[12:13], s6, v97
	v_addc_co_u32_e64 v8, s[20:21], 0, v8, s[16:17]
	v_cmp_le_u32_e64 s[16:17], s6, v98
	v_addc_co_u32_e64 v8, s[20:21], 0, v8, s[8:9]
	v_cmp_le_u32_e64 s[8:9], s6, v99
	v_addc_co_u32_e64 v8, s[20:21], 0, v8, s[12:13]
	v_cmp_le_u32_e64 s[12:13], s6, v100
	v_addc_co_u32_e64 v8, s[20:21], 0, v8, s[16:17]
	v_cmp_le_u32_e64 s[16:17], s6, v101
	v_addc_co_u32_e64 v8, s[20:21], 0, v8, s[8:9]
	v_cmp_le_u32_e64 s[8:9], s6, v102
	v_addc_co_u32_e64 v8, s[20:21], 0, v8, s[12:13]
	v_cmp_le_u32_e64 s[12:13], s6, v103
	v_addc_co_u32_e64 v8, s[20:21], 0, v8, s[16:17]
	v_cmp_le_u32_e64 s[16:17], s6, v104
	v_addc_co_u32_e64 v8, s[20:21], 0, v8, s[8:9]
	v_cmp_le_u32_e64 s[8:9], s6, v105
	v_addc_co_u32_e64 v8, s[20:21], 0, v8, s[12:13]
	v_cmp_le_u32_e64 s[12:13], s6, v106
	v_addc_co_u32_e64 v8, s[20:21], 0, v8, s[16:17]
	v_cmp_le_u32_e64 s[16:17], s6, v107
	v_addc_co_u32_e64 v8, s[20:21], 0, v8, s[8:9]
	v_cmp_le_u32_e64 s[8:9], s6, v108
	v_addc_co_u32_e64 v8, s[20:21], 0, v8, s[12:13]
	v_cmp_le_u32_e64 s[12:13], s6, v109
	v_addc_co_u32_e64 v8, s[20:21], 0, v8, s[16:17]
	v_cmp_le_u32_e64 s[16:17], s6, v110
	v_addc_co_u32_e64 v8, s[20:21], 0, v8, s[8:9]
	v_cmp_le_u32_e64 s[8:9], s6, v112
	v_addc_co_u32_e64 v8, s[20:21], 0, v8, s[12:13]
	v_cmp_le_u32_e64 s[12:13], s6, v114
	v_addc_co_u32_e64 v8, s[20:21], 0, v8, s[16:17]
	v_addc_co_u32_e64 v8, s[20:21], 0, v8, s[8:9]
	v_addc_co_u32_e64 v8, s[20:21], 0, v8, s[12:13]
	v_and_b32_e32 v9, 16, v8
	v_cmp_ne_u32_e64 s[22:23], 0, v9
	v_and_b32_e32 v9, 8, v8
	v_cmp_ne_u32_e64 s[18:19], 0, v9
	v_and_b32_e32 v9, 4, v8
	v_cmp_ne_u32_e64 s[16:17], 0, v9
	v_and_b32_e32 v9, 2, v8
	v_cmp_ne_u32_e64 s[12:13], 0, v9
	v_and_b32_e32 v9, 1, v8
	v_cmp_ne_u32_e64 s[8:9], 0, v9
	s_bcnt1_i32_b64 s7, s[22:23]
	s_bcnt1_i32_b64 s3, s[18:19]
	s_lshl1_add_u32 s7, s7, s3
	s_bcnt1_i32_b64 s3, s[16:17]
	s_lshl1_add_u32 s7, s7, s3
	s_bcnt1_i32_b64 s3, s[12:13]
	s_lshl1_add_u32 s7, s7, s3
	s_bcnt1_i32_b64 s3, s[8:9]
	s_lshl1_add_u32 s7, s7, s3
	s_cmp_lg_u32 s5, 0
	s_cbranch_scc1 .Ltk3_c20
	s_cmpk_ge_u32 s7, 0x100
	s_cbranch_scc1 .Ltk3_f20
	s_mov_b32 s6, s10
	s_mov_b32 s5, 1
	s_branch .Ltk3_b20
